# P1 epilogue stores sc1 (write-through) instead of nt
# speedup vs baseline: 1.0040x; 1.0040x over previous
.LBB0_187:
	s_or_b64 exec, exec, s[6:7]
	v_lshlrev_b64 v[224:225], 7, v[206:207]
	v_ashrrev_i32_e32 v223, 31, v222
	v_lshl_add_u64 v[224:225], s[12:13], 0, v[224:225]
	v_lshl_add_u64 v[224:225], v[222:223], 2, v[224:225]
	global_store_dwordx4 v[224:225], v[2:5], off sc1
	global_store_dwordx4 v[224:225], v[6:9], off offset:16 sc1
	s_and_saveexec_b64 s[6:7], s[4:5]
	s_xor_b64 s[6:7], exec, s[6:7]
	s_cbranch_execz .LBB0_189
	v_mul_f32_e32 v2, 0xbfb8aa3b, v134
	v_mul_f32_e32 v3, 0xbfb8aa3b, v135
	v_mul_f32_e32 v4, 0xbfb8aa3b, v136
	v_mul_f32_e32 v5, 0xbfb8aa3b, v137
	v_mul_f32_e32 v6, 0xbfb8aa3b, v146
	v_mul_f32_e32 v7, 0xbfb8aa3b, v147
	v_mul_f32_e32 v8, 0xbfb8aa3b, v148
	v_mul_f32_e32 v9, 0xbfb8aa3b, v149
	v_exp_f32_e32 v2, v2
	v_exp_f32_e32 v3, v3
	v_exp_f32_e32 v4, v4
	v_exp_f32_e32 v5, v5
	v_exp_f32_e32 v6, v6
	v_exp_f32_e32 v7, v7
	v_exp_f32_e32 v8, v8
	v_exp_f32_e32 v9, v9
	v_add_f32_e32 v2, 1.0, v2
	v_add_f32_e32 v3, 1.0, v3
	v_add_f32_e32 v4, 1.0, v4
	v_add_f32_e32 v5, 1.0, v5
	v_add_f32_e32 v6, 1.0, v6
	v_add_f32_e32 v7, 1.0, v7
	v_add_f32_e32 v8, 1.0, v8
	v_add_f32_e32 v9, 1.0, v9
	v_rcp_f32_e32 v2, v2
	v_rcp_f32_e32 v3, v3
	v_rcp_f32_e32 v4, v4
	v_rcp_f32_e32 v5, v5
	v_rcp_f32_e32 v6, v6
	v_rcp_f32_e32 v7, v7
	v_rcp_f32_e32 v8, v8
	v_rcp_f32_e32 v9, v9

.LBB0_191:
	s_or_b64 exec, exec, s[6:7]
	v_lshlrev_b64 v[224:225], 7, v[208:209]
	v_lshl_add_u64 v[224:225], s[12:13], 0, v[224:225]
	v_lshl_add_u64 v[224:225], v[222:223], 2, v[224:225]
	global_store_dwordx4 v[224:225], v[2:5], off sc1
	global_store_dwordx4 v[224:225], v[6:9], off offset:16 sc1
	s_and_saveexec_b64 s[6:7], s[4:5]
	s_xor_b64 s[6:7], exec, s[6:7]
	s_cbranch_execz .LBB0_193
	v_mul_f32_e32 v2, 0xbfb8aa3b, v158
	v_mul_f32_e32 v3, 0xbfb8aa3b, v159
	v_mul_f32_e32 v4, 0xbfb8aa3b, v160
	v_mul_f32_e32 v5, 0xbfb8aa3b, v161
	v_mul_f32_e32 v6, 0xbfb8aa3b, v114
	v_mul_f32_e32 v7, 0xbfb8aa3b, v115
	v_mul_f32_e32 v8, 0xbfb8aa3b, v116
	v_mul_f32_e32 v9, 0xbfb8aa3b, v117
	v_exp_f32_e32 v2, v2
	v_exp_f32_e32 v3, v3
	v_exp_f32_e32 v4, v4
	v_exp_f32_e32 v5, v5
	v_exp_f32_e32 v6, v6
	v_exp_f32_e32 v7, v7
	v_exp_f32_e32 v8, v8
	v_exp_f32_e32 v9, v9
	v_add_f32_e32 v2, 1.0, v2
	v_add_f32_e32 v3, 1.0, v3
	v_add_f32_e32 v4, 1.0, v4
	v_add_f32_e32 v5, 1.0, v5
	v_add_f32_e32 v6, 1.0, v6
	v_add_f32_e32 v7, 1.0, v7
	v_add_f32_e32 v8, 1.0, v8
	v_add_f32_e32 v9, 1.0, v9
	v_rcp_f32_e32 v2, v2
	v_rcp_f32_e32 v3, v3
	v_rcp_f32_e32 v4, v4
	v_rcp_f32_e32 v5, v5
	v_rcp_f32_e32 v6, v6
	v_rcp_f32_e32 v7, v7
	v_rcp_f32_e32 v8, v8
	v_rcp_f32_e32 v9, v9

.LBB0_195:
	s_or_b64 exec, exec, s[6:7]
	v_lshlrev_b64 v[224:225], 7, v[210:211]
	v_lshl_add_u64 v[224:225], s[12:13], 0, v[224:225]
	v_lshl_add_u64 v[224:225], v[222:223], 2, v[224:225]
	global_store_dwordx4 v[224:225], v[2:5], off sc1
	global_store_dwordx4 v[224:225], v[6:9], off offset:16 sc1
	s_and_saveexec_b64 s[6:7], s[4:5]
	s_xor_b64 s[6:7], exec, s[6:7]
	s_cbranch_execz .LBB0_197
	v_mul_f32_e32 v2, 0xbfb8aa3b, v126
	v_mul_f32_e32 v3, 0xbfb8aa3b, v127
	v_mul_f32_e32 v4, 0xbfb8aa3b, v128
	v_mul_f32_e32 v5, 0xbfb8aa3b, v129
	v_mul_f32_e32 v6, 0xbfb8aa3b, v138
	v_mul_f32_e32 v7, 0xbfb8aa3b, v139
	v_mul_f32_e32 v8, 0xbfb8aa3b, v140
	v_mul_f32_e32 v9, 0xbfb8aa3b, v141
	v_exp_f32_e32 v2, v2
	v_exp_f32_e32 v3, v3
	v_exp_f32_e32 v4, v4
	v_exp_f32_e32 v5, v5
	v_exp_f32_e32 v6, v6
	v_exp_f32_e32 v7, v7
	v_exp_f32_e32 v8, v8
	v_exp_f32_e32 v9, v9
	v_add_f32_e32 v2, 1.0, v2
	v_add_f32_e32 v3, 1.0, v3
	v_add_f32_e32 v4, 1.0, v4
	v_add_f32_e32 v5, 1.0, v5
	v_add_f32_e32 v6, 1.0, v6
	v_add_f32_e32 v7, 1.0, v7
	v_add_f32_e32 v8, 1.0, v8
	v_add_f32_e32 v9, 1.0, v9
	v_rcp_f32_e32 v2, v2
	v_rcp_f32_e32 v3, v3
	v_rcp_f32_e32 v4, v4
	v_rcp_f32_e32 v5, v5
	v_rcp_f32_e32 v6, v6
	v_rcp_f32_e32 v7, v7
	v_rcp_f32_e32 v8, v8
	v_rcp_f32_e32 v9, v9

.LBB0_199:
	s_or_b64 exec, exec, s[6:7]
	v_lshlrev_b64 v[224:225], 7, v[212:213]
	v_lshl_add_u64 v[224:225], s[12:13], 0, v[224:225]
	v_lshl_add_u64 v[224:225], v[222:223], 2, v[224:225]
	global_store_dwordx4 v[224:225], v[2:5], off sc1
	global_store_dwordx4 v[224:225], v[6:9], off offset:16 sc1
	s_and_saveexec_b64 s[6:7], s[4:5]
	s_xor_b64 s[6:7], exec, s[6:7]
	s_cbranch_execz .LBB0_201
	v_mul_f32_e32 v2, 0xbfb8aa3b, v66
	v_mul_f32_e32 v3, 0xbfb8aa3b, v67
	v_mul_f32_e32 v4, 0xbfb8aa3b, v68
	v_mul_f32_e32 v5, 0xbfb8aa3b, v69
	v_mul_f32_e32 v6, 0xbfb8aa3b, v70
	v_mul_f32_e32 v7, 0xbfb8aa3b, v71
	v_mul_f32_e32 v8, 0xbfb8aa3b, v72
	v_mul_f32_e32 v9, 0xbfb8aa3b, v73
	v_exp_f32_e32 v2, v2
	v_exp_f32_e32 v3, v3
	v_exp_f32_e32 v4, v4
	v_exp_f32_e32 v5, v5
	v_exp_f32_e32 v6, v6
	v_exp_f32_e32 v7, v7
	v_exp_f32_e32 v8, v8
	v_exp_f32_e32 v9, v9
	v_add_f32_e32 v2, 1.0, v2
	v_add_f32_e32 v3, 1.0, v3
	v_add_f32_e32 v4, 1.0, v4
	v_add_f32_e32 v5, 1.0, v5
	v_add_f32_e32 v6, 1.0, v6
	v_add_f32_e32 v7, 1.0, v7
	v_add_f32_e32 v8, 1.0, v8
	v_add_f32_e32 v9, 1.0, v9
	v_rcp_f32_e32 v2, v2
	v_rcp_f32_e32 v3, v3
	v_rcp_f32_e32 v4, v4
	v_rcp_f32_e32 v5, v5
	v_rcp_f32_e32 v6, v6
	v_rcp_f32_e32 v7, v7
	v_rcp_f32_e32 v8, v8
	v_rcp_f32_e32 v9, v9

.LBB0_203:
	s_or_b64 exec, exec, s[6:7]
	v_lshlrev_b64 v[224:225], 7, v[214:215]
	v_lshl_add_u64 v[224:225], s[12:13], 0, v[224:225]
	v_lshl_add_u64 v[224:225], v[222:223], 2, v[224:225]
	global_store_dwordx4 v[224:225], v[2:5], off sc1
	global_store_dwordx4 v[224:225], v[6:9], off offset:16 sc1
	s_and_saveexec_b64 s[6:7], s[4:5]
	s_xor_b64 s[6:7], exec, s[6:7]
	s_cbranch_execz .LBB0_205
	v_mul_f32_e32 v2, 0xbfb8aa3b, v74
	v_mul_f32_e32 v3, 0xbfb8aa3b, v75
	v_mul_f32_e32 v4, 0xbfb8aa3b, v76
	v_mul_f32_e32 v5, 0xbfb8aa3b, v77
	v_mul_f32_e32 v6, 0xbfb8aa3b, v78
	v_mul_f32_e32 v7, 0xbfb8aa3b, v79
	v_mul_f32_e32 v8, 0xbfb8aa3b, v80
	v_mul_f32_e32 v9, 0xbfb8aa3b, v81
	v_exp_f32_e32 v2, v2
	v_exp_f32_e32 v3, v3
	v_exp_f32_e32 v4, v4
	v_exp_f32_e32 v5, v5
	v_exp_f32_e32 v6, v6
	v_exp_f32_e32 v7, v7
	v_exp_f32_e32 v8, v8
	v_exp_f32_e32 v9, v9
	v_add_f32_e32 v2, 1.0, v2
	v_add_f32_e32 v3, 1.0, v3
	v_add_f32_e32 v4, 1.0, v4
	v_add_f32_e32 v5, 1.0, v5
	v_add_f32_e32 v6, 1.0, v6
	v_add_f32_e32 v7, 1.0, v7
	v_add_f32_e32 v8, 1.0, v8
	v_add_f32_e32 v9, 1.0, v9
	v_rcp_f32_e32 v2, v2
	v_rcp_f32_e32 v3, v3
	v_rcp_f32_e32 v4, v4
	v_rcp_f32_e32 v5, v5
	v_rcp_f32_e32 v6, v6
	v_rcp_f32_e32 v7, v7
	v_rcp_f32_e32 v8, v8
	v_rcp_f32_e32 v9, v9

.LBB0_207:
	s_or_b64 exec, exec, s[6:7]
	v_lshlrev_b64 v[224:225], 7, v[216:217]
	v_lshl_add_u64 v[224:225], s[12:13], 0, v[224:225]
	v_lshl_add_u64 v[224:225], v[222:223], 2, v[224:225]
	global_store_dwordx4 v[224:225], v[2:5], off sc1
	global_store_dwordx4 v[224:225], v[6:9], off offset:16 sc1
	s_and_saveexec_b64 s[6:7], s[4:5]
	s_xor_b64 s[6:7], exec, s[6:7]
	s_cbranch_execz .LBB0_209
	v_mul_f32_e32 v2, 0xbfb8aa3b, v82
	v_mul_f32_e32 v3, 0xbfb8aa3b, v83
	v_mul_f32_e32 v4, 0xbfb8aa3b, v84
	v_mul_f32_e32 v5, 0xbfb8aa3b, v85
	v_mul_f32_e32 v6, 0xbfb8aa3b, v86
	v_mul_f32_e32 v7, 0xbfb8aa3b, v87
	v_mul_f32_e32 v8, 0xbfb8aa3b, v88
	v_mul_f32_e32 v9, 0xbfb8aa3b, v89
	v_exp_f32_e32 v2, v2
	v_exp_f32_e32 v3, v3
	v_exp_f32_e32 v4, v4
	v_exp_f32_e32 v5, v5
	v_exp_f32_e32 v6, v6
	v_exp_f32_e32 v7, v7
	v_exp_f32_e32 v8, v8
	v_exp_f32_e32 v9, v9
	v_add_f32_e32 v2, 1.0, v2
	v_add_f32_e32 v3, 1.0, v3
	v_add_f32_e32 v4, 1.0, v4
	v_add_f32_e32 v5, 1.0, v5
	v_add_f32_e32 v6, 1.0, v6
	v_add_f32_e32 v7, 1.0, v7
	v_add_f32_e32 v8, 1.0, v8
	v_add_f32_e32 v9, 1.0, v9
	v_rcp_f32_e32 v2, v2
	v_rcp_f32_e32 v3, v3
	v_rcp_f32_e32 v4, v4
	v_rcp_f32_e32 v5, v5
	v_rcp_f32_e32 v6, v6
	v_rcp_f32_e32 v7, v7
	v_rcp_f32_e32 v8, v8
	v_rcp_f32_e32 v9, v9

.LBB0_211:
	s_or_b64 exec, exec, s[6:7]
	v_lshlrev_b64 v[224:225], 7, v[218:219]
	v_lshl_add_u64 v[224:225], s[12:13], 0, v[224:225]
	v_lshl_add_u64 v[224:225], v[222:223], 2, v[224:225]
	global_store_dwordx4 v[224:225], v[2:5], off sc1
	global_store_dwordx4 v[224:225], v[6:9], off offset:16 sc1
	s_and_saveexec_b64 s[6:7], s[4:5]
	s_xor_b64 s[6:7], exec, s[6:7]
	s_cbranch_execz .LBB0_213
	v_mul_f32_e32 v2, 0xbfb8aa3b, v90
	v_mul_f32_e32 v3, 0xbfb8aa3b, v91
	v_mul_f32_e32 v4, 0xbfb8aa3b, v92
	v_mul_f32_e32 v5, 0xbfb8aa3b, v93
	v_mul_f32_e32 v6, 0xbfb8aa3b, v94
	v_mul_f32_e32 v7, 0xbfb8aa3b, v95
	v_mul_f32_e32 v8, 0xbfb8aa3b, v96
	v_mul_f32_e32 v9, 0xbfb8aa3b, v97
	v_exp_f32_e32 v2, v2
	v_exp_f32_e32 v3, v3
	v_exp_f32_e32 v4, v4
	v_exp_f32_e32 v5, v5
	v_exp_f32_e32 v6, v6
	v_exp_f32_e32 v7, v7
	v_exp_f32_e32 v8, v8
	v_exp_f32_e32 v9, v9
	v_add_f32_e32 v2, 1.0, v2
	v_add_f32_e32 v3, 1.0, v3
	v_add_f32_e32 v4, 1.0, v4
	v_add_f32_e32 v5, 1.0, v5
	v_add_f32_e32 v6, 1.0, v6
	v_add_f32_e32 v7, 1.0, v7
	v_add_f32_e32 v8, 1.0, v8
	v_add_f32_e32 v9, 1.0, v9
	v_rcp_f32_e32 v2, v2
	v_rcp_f32_e32 v3, v3
	v_rcp_f32_e32 v4, v4
	v_rcp_f32_e32 v5, v5
	v_rcp_f32_e32 v6, v6
	v_rcp_f32_e32 v7, v7
	v_rcp_f32_e32 v8, v8
	v_rcp_f32_e32 v9, v9

.LBB0_215:
	s_or_b64 exec, exec, s[6:7]
	s_waitcnt vmcnt(0)
	v_lshlrev_b64 v[10:11], 7, v[220:221]
	v_lshl_add_u64 v[10:11], s[12:13], 0, v[10:11]
	v_lshl_add_u64 v[10:11], v[222:223], 2, v[10:11]
	global_store_dwordx4 v[10:11], v[2:5], off sc1
	global_store_dwordx4 v[10:11], v[6:9], off offset:16 sc1

.LBB0_217:
	s_andn2_b64 vcc, exec, s[6:7]
	s_cbranch_vccnz .LBB0_219
	v_mul_f32_e32 v8, 0xbfb8aa3b, v122
	v_exp_f32_e32 v8, v8
	v_mul_f32_e32 v9, 0xbfb8aa3b, v123
	v_exp_f32_e32 v9, v9
	v_mul_f32_e32 v4, 0xbfb8aa3b, v106
	v_add_f32_e32 v8, 1.0, v8
	s_waitcnt vmcnt(0)
	v_rcp_f32_e32 v10, v8
	v_add_f32_e32 v8, 1.0, v9
	v_mul_f32_e32 v9, 0xbfb8aa3b, v124
	v_mul_f32_e32 v5, 0xbfb8aa3b, v107
	v_mul_f32_e32 v6, 0xbfb8aa3b, v108
	v_mul_f32_e32 v7, 0xbfb8aa3b, v109
	v_exp_f32_e32 v9, v9
	v_mul_f32_e32 v11, 0xbfb8aa3b, v125
	s_sub_i32 s31, s29, 22
	v_exp_f32_e32 v4, v4
	v_exp_f32_e32 v5, v5
	v_exp_f32_e32 v6, v6
	v_exp_f32_e32 v7, v7
	v_exp_f32_e32 v11, v11
	s_lshr_b32 s8, s31, 3
	s_lshl_b64 s[6:7], s[8:9], 26
	s_add_u32 s6, s80, s6
	v_rcp_f32_e32 v12, v8
	v_add_f32_e32 v8, 1.0, v9
	s_addc_u32 s7, s81, s7
	s_lshl_b32 s8, s31, 8
	v_add_f32_e32 v4, 1.0, v4
	v_add_f32_e32 v5, 1.0, v5
	v_add_f32_e32 v6, 1.0, v6
	v_add_f32_e32 v7, 1.0, v7
	v_rcp_f32_e32 v13, v8
	v_add_f32_e32 v8, 1.0, v11
	s_and_b32 s8, s8, 0x600
	v_mov_b32_e32 v2, v235
	v_mov_b32_e32 v3, v240
	v_rcp_f32_e32 v4, v4
	v_rcp_f32_e32 v5, v5
	v_rcp_f32_e32 v6, v6
	v_rcp_f32_e32 v7, v7
	v_rcp_f32_e32 v11, v8
	s_add_u32 s6, s6, s8
	s_addc_u32 s7, s7, 0
	v_ashrrev_i32_e32 v3, 31, v2
	v_lshl_add_u64 v[2:3], v[2:3], 1, s[6:7]
	v_lshl_add_u64 v[8:9], v[2:3], 0, v[64:65]
	v_cvt_pk_bf16_f32 v4, v4, v5
	v_cvt_pk_bf16_f32 v5, v6, v7
	v_cvt_pk_bf16_f32 v6, v10, v12
	v_cvt_pk_bf16_f32 v7, v13, v11
	global_store_dwordx4 v[8:9], v[4:7], off sc1
	v_mul_f32_e32 v8, 0xbfb8aa3b, v146
	v_mul_f32_e32 v10, 0xbfb8aa3b, v134
	v_exp_f32_e32 v8, v8
	v_mul_f32_e32 v9, 0xbfb8aa3b, v147
	v_exp_f32_e32 v10, v10
	v_mul_f32_e32 v11, 0xbfb8aa3b, v135
	v_exp_f32_e32 v9, v9
	v_exp_f32_e32 v11, v11
	v_add_f32_e32 v8, 1.0, v8
	v_add_f32_e32 v4, 1.0, v10
	v_rcp_f32_e32 v10, v8
	v_add_f32_e32 v8, 1.0, v9
	v_mul_f32_e32 v9, 0xbfb8aa3b, v148
	v_add_f32_e32 v5, 1.0, v11
	v_mul_f32_e32 v6, 0xbfb8aa3b, v136
	v_mul_f32_e32 v7, 0xbfb8aa3b, v137
	v_exp_f32_e32 v9, v9
	v_mul_f32_e32 v11, 0xbfb8aa3b, v149
	v_exp_f32_e32 v6, v6
	v_exp_f32_e32 v7, v7
	v_exp_f32_e32 v11, v11
	v_rcp_f32_e32 v12, v8
	v_add_f32_e32 v8, 1.0, v9
	v_add_f32_e32 v6, 1.0, v6
	v_add_f32_e32 v7, 1.0, v7
	v_rcp_f32_e32 v13, v8
	v_add_f32_e32 v8, 1.0, v11
	v_rcp_f32_e32 v4, v4
	v_rcp_f32_e32 v5, v5
	v_rcp_f32_e32 v6, v6
	v_rcp_f32_e32 v7, v7
	v_rcp_f32_e32 v11, v8
	v_lshl_add_u64 v[8:9], v[2:3], 0, v[62:63]
	v_cvt_pk_bf16_f32 v4, v4, v5
	v_cvt_pk_bf16_f32 v5, v6, v7
	v_cvt_pk_bf16_f32 v6, v10, v12
	v_cvt_pk_bf16_f32 v7, v13, v11
	global_store_dwordx4 v[8:9], v[4:7], off sc1
	v_mul_f32_e32 v8, 0xbfb8aa3b, v114
	v_mul_f32_e32 v10, 0xbfb8aa3b, v158
	v_exp_f32_e32 v8, v8
	v_mul_f32_e32 v9, 0xbfb8aa3b, v115
	v_exp_f32_e32 v10, v10
	v_mul_f32_e32 v11, 0xbfb8aa3b, v159
	v_exp_f32_e32 v9, v9
	v_exp_f32_e32 v11, v11
	v_add_f32_e32 v8, 1.0, v8
	v_add_f32_e32 v4, 1.0, v10
	v_rcp_f32_e32 v10, v8
	v_add_f32_e32 v8, 1.0, v9
	v_mul_f32_e32 v9, 0xbfb8aa3b, v116
	v_add_f32_e32 v5, 1.0, v11
	v_mul_f32_e32 v6, 0xbfb8aa3b, v160
	v_mul_f32_e32 v7, 0xbfb8aa3b, v161
	v_exp_f32_e32 v9, v9
	v_mul_f32_e32 v11, 0xbfb8aa3b, v117
	v_exp_f32_e32 v6, v6
	v_exp_f32_e32 v7, v7
	v_exp_f32_e32 v11, v11
	v_rcp_f32_e32 v12, v8
	v_add_f32_e32 v8, 1.0, v9
	v_add_f32_e32 v6, 1.0, v6
	v_add_f32_e32 v7, 1.0, v7
	v_rcp_f32_e32 v13, v8
	v_add_f32_e32 v8, 1.0, v11
	v_rcp_f32_e32 v4, v4
	v_rcp_f32_e32 v5, v5
	v_rcp_f32_e32 v6, v6
	v_rcp_f32_e32 v7, v7
	v_rcp_f32_e32 v11, v8
	v_lshl_add_u64 v[8:9], v[2:3], 0, v[60:61]
	v_cvt_pk_bf16_f32 v4, v4, v5
	v_cvt_pk_bf16_f32 v5, v6, v7
	v_cvt_pk_bf16_f32 v6, v10, v12
	v_cvt_pk_bf16_f32 v7, v13, v11
	global_store_dwordx4 v[8:9], v[4:7], off sc1
	v_mul_f32_e32 v8, 0xbfb8aa3b, v138
	v_mul_f32_e32 v10, 0xbfb8aa3b, v126
	v_exp_f32_e32 v8, v8
	v_mul_f32_e32 v9, 0xbfb8aa3b, v139
	v_exp_f32_e32 v10, v10
	v_mul_f32_e32 v11, 0xbfb8aa3b, v127
	v_exp_f32_e32 v9, v9
	v_exp_f32_e32 v11, v11
	v_add_f32_e32 v8, 1.0, v8
	v_add_f32_e32 v4, 1.0, v10
	v_rcp_f32_e32 v10, v8
	v_add_f32_e32 v8, 1.0, v9
	v_mul_f32_e32 v9, 0xbfb8aa3b, v140
	v_add_f32_e32 v5, 1.0, v11
	v_mul_f32_e32 v6, 0xbfb8aa3b, v128
	v_mul_f32_e32 v7, 0xbfb8aa3b, v129
	v_exp_f32_e32 v9, v9
	v_mul_f32_e32 v11, 0xbfb8aa3b, v141
	v_exp_f32_e32 v6, v6
	v_exp_f32_e32 v7, v7
	v_exp_f32_e32 v11, v11
	v_rcp_f32_e32 v12, v8
	v_add_f32_e32 v8, 1.0, v9
	v_add_f32_e32 v6, 1.0, v6
	v_add_f32_e32 v7, 1.0, v7
	v_rcp_f32_e32 v13, v8
	v_add_f32_e32 v8, 1.0, v11
	v_rcp_f32_e32 v4, v4
	v_rcp_f32_e32 v5, v5
	v_rcp_f32_e32 v6, v6
	v_rcp_f32_e32 v7, v7
	v_rcp_f32_e32 v11, v8
	v_lshl_add_u64 v[8:9], v[2:3], 0, v[58:59]
	v_cvt_pk_bf16_f32 v4, v4, v5
	v_cvt_pk_bf16_f32 v5, v6, v7
	v_cvt_pk_bf16_f32 v6, v10, v12
	v_cvt_pk_bf16_f32 v7, v13, v11
	global_store_dwordx4 v[8:9], v[4:7], off sc1
	v_mul_f32_e32 v8, 0xbfb8aa3b, v70
	v_mul_f32_e32 v10, 0xbfb8aa3b, v66
	v_exp_f32_e32 v8, v8
	v_mul_f32_e32 v9, 0xbfb8aa3b, v71
	v_exp_f32_e32 v10, v10
	v_mul_f32_e32 v11, 0xbfb8aa3b, v67
	v_exp_f32_e32 v9, v9
	v_exp_f32_e32 v11, v11
	v_add_f32_e32 v8, 1.0, v8
	v_add_f32_e32 v4, 1.0, v10
	v_rcp_f32_e32 v10, v8
	v_add_f32_e32 v8, 1.0, v9
	v_mul_f32_e32 v9, 0xbfb8aa3b, v72
	v_add_f32_e32 v5, 1.0, v11
	v_mul_f32_e32 v6, 0xbfb8aa3b, v68
	v_mul_f32_e32 v7, 0xbfb8aa3b, v69
	v_exp_f32_e32 v9, v9
	v_mul_f32_e32 v11, 0xbfb8aa3b, v73
	v_exp_f32_e32 v6, v6
	v_exp_f32_e32 v7, v7
	v_exp_f32_e32 v11, v11
	v_rcp_f32_e32 v12, v8
	v_add_f32_e32 v8, 1.0, v9
	v_add_f32_e32 v6, 1.0, v6
	v_add_f32_e32 v7, 1.0, v7
	v_rcp_f32_e32 v13, v8
	v_add_f32_e32 v8, 1.0, v11
	v_rcp_f32_e32 v4, v4
	v_rcp_f32_e32 v5, v5
	v_rcp_f32_e32 v6, v6
	v_rcp_f32_e32 v7, v7
	v_rcp_f32_e32 v11, v8
	v_lshl_add_u64 v[8:9], v[2:3], 0, v[56:57]
	v_cvt_pk_bf16_f32 v4, v4, v5
	v_cvt_pk_bf16_f32 v5, v6, v7
	v_cvt_pk_bf16_f32 v6, v10, v12
	v_cvt_pk_bf16_f32 v7, v13, v11
	global_store_dwordx4 v[8:9], v[4:7], off sc1
	v_mul_f32_e32 v8, 0xbfb8aa3b, v78
	v_mul_f32_e32 v10, 0xbfb8aa3b, v74
	v_exp_f32_e32 v8, v8
	v_mul_f32_e32 v9, 0xbfb8aa3b, v79
	v_exp_f32_e32 v10, v10
	v_mul_f32_e32 v11, 0xbfb8aa3b, v75
	v_exp_f32_e32 v9, v9
	v_exp_f32_e32 v11, v11
	v_add_f32_e32 v8, 1.0, v8
	v_add_f32_e32 v4, 1.0, v10
	v_rcp_f32_e32 v10, v8
	v_add_f32_e32 v8, 1.0, v9
	v_mul_f32_e32 v9, 0xbfb8aa3b, v80
	v_add_f32_e32 v5, 1.0, v11
	v_mul_f32_e32 v6, 0xbfb8aa3b, v76
	v_mul_f32_e32 v7, 0xbfb8aa3b, v77
	v_exp_f32_e32 v9, v9
	v_mul_f32_e32 v11, 0xbfb8aa3b, v81
	v_exp_f32_e32 v6, v6
	v_exp_f32_e32 v7, v7
	v_exp_f32_e32 v11, v11
	v_rcp_f32_e32 v12, v8
	v_add_f32_e32 v8, 1.0, v9
	v_add_f32_e32 v6, 1.0, v6
	v_add_f32_e32 v7, 1.0, v7
	v_rcp_f32_e32 v13, v8
	v_add_f32_e32 v8, 1.0, v11
	v_rcp_f32_e32 v4, v4
	v_rcp_f32_e32 v5, v5
	v_rcp_f32_e32 v6, v6
	v_rcp_f32_e32 v7, v7
	v_rcp_f32_e32 v11, v8
	v_lshl_add_u64 v[8:9], v[2:3], 0, v[54:55]
	v_cvt_pk_bf16_f32 v4, v4, v5
	v_cvt_pk_bf16_f32 v5, v6, v7
	v_cvt_pk_bf16_f32 v6, v10, v12
	v_cvt_pk_bf16_f32 v7, v13, v11
	global_store_dwordx4 v[8:9], v[4:7], off sc1
	v_mul_f32_e32 v8, 0xbfb8aa3b, v86
	v_mul_f32_e32 v10, 0xbfb8aa3b, v82
	v_exp_f32_e32 v8, v8
	v_mul_f32_e32 v9, 0xbfb8aa3b, v87
	v_exp_f32_e32 v10, v10
	v_mul_f32_e32 v11, 0xbfb8aa3b, v83
	v_exp_f32_e32 v9, v9
	v_exp_f32_e32 v11, v11
	v_add_f32_e32 v8, 1.0, v8
	v_add_f32_e32 v4, 1.0, v10
	v_rcp_f32_e32 v10, v8
	v_add_f32_e32 v8, 1.0, v9
	v_mul_f32_e32 v9, 0xbfb8aa3b, v88
	v_add_f32_e32 v5, 1.0, v11
	v_mul_f32_e32 v6, 0xbfb8aa3b, v84
	v_mul_f32_e32 v7, 0xbfb8aa3b, v85
	v_exp_f32_e32 v9, v9
	v_mul_f32_e32 v11, 0xbfb8aa3b, v89
	v_exp_f32_e32 v6, v6
	v_exp_f32_e32 v7, v7
	v_exp_f32_e32 v11, v11
	v_rcp_f32_e32 v12, v8
	v_add_f32_e32 v8, 1.0, v9
	v_add_f32_e32 v6, 1.0, v6
	v_add_f32_e32 v7, 1.0, v7
	v_rcp_f32_e32 v13, v8
	v_add_f32_e32 v8, 1.0, v11
	v_rcp_f32_e32 v4, v4
	v_rcp_f32_e32 v5, v5
	v_rcp_f32_e32 v6, v6
	v_rcp_f32_e32 v7, v7
	v_rcp_f32_e32 v11, v8
	v_lshl_add_u64 v[8:9], v[2:3], 0, v[52:53]
	v_cvt_pk_bf16_f32 v4, v4, v5
	v_cvt_pk_bf16_f32 v5, v6, v7
	v_cvt_pk_bf16_f32 v6, v10, v12
	v_cvt_pk_bf16_f32 v7, v13, v11
	global_store_dwordx4 v[8:9], v[4:7], off sc1
	v_mul_f32_e32 v10, 0xbfb8aa3b, v90
	v_exp_f32_e32 v10, v10
	v_mul_f32_e32 v6, 0xbfb8aa3b, v92
	v_exp_f32_e32 v6, v6
	v_mul_f32_e32 v7, 0xbfb8aa3b, v93
	v_exp_f32_e32 v7, v7
	v_mul_f32_e32 v11, 0xbfb8aa3b, v91
	v_add_f32_e32 v6, 1.0, v6
	v_rcp_f32_e32 v8, v6
	v_add_f32_e32 v6, 1.0, v7
	v_mul_f32_e32 v7, 0xbfb8aa3b, v94
	v_exp_f32_e32 v7, v7
	v_mul_f32_e32 v9, 0xbfb8aa3b, v95
	v_exp_f32_e32 v11, v11
	v_exp_f32_e32 v9, v9
	v_add_f32_e32 v4, 1.0, v10
	v_rcp_f32_e32 v10, v6
	v_add_f32_e32 v6, 1.0, v7
	v_mul_f32_e32 v7, 0xbfb8aa3b, v96
	v_add_f32_e32 v5, 1.0, v11
	v_rcp_f32_e32 v11, v6
	v_add_f32_e32 v6, 1.0, v9
	v_exp_f32_e32 v7, v7
	v_mul_f32_e32 v9, 0xbfb8aa3b, v97
	v_exp_f32_e32 v9, v9
	v_rcp_f32_e32 v12, v6
	v_add_f32_e32 v6, 1.0, v7
	v_rcp_f32_e32 v13, v6
	v_add_f32_e32 v6, 1.0, v9
	v_rcp_f32_e32 v4, v4
	v_rcp_f32_e32 v5, v5
	v_rcp_f32_e32 v9, v6
	v_lshl_add_u64 v[6:7], v[2:3], 0, v[50:51]
	v_cvt_pk_bf16_f32 v3, v8, v10
	v_cvt_pk_bf16_f32 v2, v4, v5
	v_cvt_pk_bf16_f32 v4, v11, v12
	v_cvt_pk_bf16_f32 v5, v13, v9
	global_store_dwordx4 v[6:7], v[2:5], off sc1

.LBB0_220:
	s_andn2_b64 vcc, exec, s[6:7]
	s_cbranch_vccnz .LBB0_222
	s_add_i32 s31, s29, -10
	s_lshr_b32 s8, s31, 2
	s_lshl_b64 s[6:7], s[8:9], 25
	s_add_u32 s6, s76, s6
	s_addc_u32 s7, s77, s7
	s_lshl_b32 s8, s31, 8
	s_and_b32 s8, s8, 0x200
	v_mov_b32_e32 v2, v235
	v_mov_b32_e32 v3, v240
	s_add_u32 s6, s6, s8
	s_addc_u32 s7, s7, 0
	v_ashrrev_i32_e32 v3, 31, v2
	v_lshl_add_u64 v[6:7], v[2:3], 1, s[6:7]
	v_lshl_add_u64 v[8:9], v[6:7], 0, v[48:49]
	v_cvt_pk_bf16_f32 v2, v106, v107
	v_cvt_pk_bf16_f32 v3, v108, v109
	v_cvt_pk_bf16_f32 v4, v122, v123
	v_cvt_pk_bf16_f32 v5, v124, v125
	global_store_dwordx4 v[8:9], v[2:5], off sc1
	v_lshl_add_u64 v[8:9], v[6:7], 0, v[46:47]
	s_nop 0
	v_cvt_pk_bf16_f32 v2, v134, v135
	v_cvt_pk_bf16_f32 v3, v136, v137
	v_cvt_pk_bf16_f32 v4, v146, v147
	v_cvt_pk_bf16_f32 v5, v148, v149
	global_store_dwordx4 v[8:9], v[2:5], off sc1
	v_lshl_add_u64 v[8:9], v[6:7], 0, v[44:45]
	s_nop 0
	v_cvt_pk_bf16_f32 v2, v158, v159
	v_cvt_pk_bf16_f32 v3, v160, v161
	v_cvt_pk_bf16_f32 v4, v114, v115
	v_cvt_pk_bf16_f32 v5, v116, v117
	global_store_dwordx4 v[8:9], v[2:5], off sc1
	v_lshl_add_u64 v[8:9], v[6:7], 0, v[42:43]
	s_nop 0
	v_cvt_pk_bf16_f32 v2, v126, v127
	v_cvt_pk_bf16_f32 v3, v128, v129
	v_cvt_pk_bf16_f32 v4, v138, v139
	v_cvt_pk_bf16_f32 v5, v140, v141
	global_store_dwordx4 v[8:9], v[2:5], off sc1
	v_lshl_add_u64 v[8:9], v[6:7], 0, v[40:41]
	s_nop 0
	v_cvt_pk_bf16_f32 v2, v66, v67
	v_cvt_pk_bf16_f32 v3, v68, v69
	v_cvt_pk_bf16_f32 v4, v70, v71
	v_cvt_pk_bf16_f32 v5, v72, v73
	global_store_dwordx4 v[8:9], v[2:5], off sc1
	v_lshl_add_u64 v[8:9], v[6:7], 0, v[38:39]
	s_nop 0
	v_cvt_pk_bf16_f32 v2, v74, v75
	v_cvt_pk_bf16_f32 v3, v76, v77
	v_cvt_pk_bf16_f32 v4, v78, v79
	v_cvt_pk_bf16_f32 v5, v80, v81
	global_store_dwordx4 v[8:9], v[2:5], off sc1
	v_lshl_add_u64 v[8:9], v[6:7], 0, v[36:37]
	v_lshl_add_u64 v[6:7], v[6:7], 0, v[34:35]
	v_cvt_pk_bf16_f32 v2, v82, v83
	v_cvt_pk_bf16_f32 v3, v84, v85
	v_cvt_pk_bf16_f32 v4, v86, v87
	v_cvt_pk_bf16_f32 v5, v88, v89
	global_store_dwordx4 v[8:9], v[2:5], off sc1
	s_nop 1
	v_cvt_pk_bf16_f32 v2, v90, v91
	v_cvt_pk_bf16_f32 v3, v92, v93
	v_cvt_pk_bf16_f32 v4, v94, v95
	v_cvt_pk_bf16_f32 v5, v96, v97
	global_store_dwordx4 v[6:7], v[2:5], off sc1

.LBB0_223:
	s_andn2_b64 vcc, exec, s[6:7]
	s_cbranch_vccnz .LBB0_225
	s_lshl_b32 s8, s42, 8
	s_lshl_b64 s[6:7], s[8:9], 1
	v_mov_b32_e32 v2, v235
	v_mov_b32_e32 v3, v240
	s_add_u32 s6, s76, s6
	s_addc_u32 s7, s77, s7
	v_ashrrev_i32_e32 v3, 31, v2
	v_lshl_add_u64 v[6:7], v[2:3], 1, s[6:7]
	v_pk_mul_f32 v[2:3], v[106:107], s[26:27] op_sel_hi:[1,0]
	v_pk_mul_f32 v[4:5], v[108:109], s[26:27] op_sel_hi:[1,0]
	v_pk_mul_f32 v[8:9], v[122:123], s[26:27] op_sel_hi:[1,0]
	s_waitcnt vmcnt(0)
	v_pk_mul_f32 v[10:11], v[124:125], s[26:27] op_sel_hi:[1,0]
	v_lshl_add_u64 v[12:13], v[6:7], 0, v[48:49]
	v_cvt_pk_bf16_f32 v2, v2, v3
	v_cvt_pk_bf16_f32 v3, v4, v5
	v_cvt_pk_bf16_f32 v4, v8, v9
	v_cvt_pk_bf16_f32 v5, v10, v11
	global_store_dwordx4 v[12:13], v[2:5], off offset:-2560 sc1
	v_pk_mul_f32 v[8:9], v[146:147], s[26:27] op_sel_hi:[1,0]
	v_pk_mul_f32 v[10:11], v[148:149], s[26:27] op_sel_hi:[1,0]
	v_pk_mul_f32 v[2:3], v[134:135], s[26:27] op_sel_hi:[1,0]
	v_pk_mul_f32 v[4:5], v[136:137], s[26:27] op_sel_hi:[1,0]
	v_lshl_add_u64 v[12:13], v[6:7], 0, v[46:47]
	v_cvt_pk_bf16_f32 v2, v2, v3
	v_cvt_pk_bf16_f32 v3, v4, v5
	v_cvt_pk_bf16_f32 v4, v8, v9
	v_cvt_pk_bf16_f32 v5, v10, v11
	global_store_dwordx4 v[12:13], v[2:5], off offset:-2560 sc1
	v_pk_mul_f32 v[8:9], v[114:115], s[26:27] op_sel_hi:[1,0]
	v_pk_mul_f32 v[10:11], v[116:117], s[26:27] op_sel_hi:[1,0]
	v_pk_mul_f32 v[2:3], v[158:159], s[26:27] op_sel_hi:[1,0]
	v_pk_mul_f32 v[4:5], v[160:161], s[26:27] op_sel_hi:[1,0]
	v_lshl_add_u64 v[12:13], v[6:7], 0, v[44:45]
	v_cvt_pk_bf16_f32 v2, v2, v3
	v_cvt_pk_bf16_f32 v3, v4, v5
	v_cvt_pk_bf16_f32 v4, v8, v9
	v_cvt_pk_bf16_f32 v5, v10, v11
	global_store_dwordx4 v[12:13], v[2:5], off offset:-2560 sc1
	v_pk_mul_f32 v[8:9], v[138:139], s[26:27] op_sel_hi:[1,0]
	v_pk_mul_f32 v[10:11], v[140:141], s[26:27] op_sel_hi:[1,0]
	v_pk_mul_f32 v[2:3], v[126:127], s[26:27] op_sel_hi:[1,0]
	v_pk_mul_f32 v[4:5], v[128:129], s[26:27] op_sel_hi:[1,0]
	v_lshl_add_u64 v[12:13], v[6:7], 0, v[42:43]
	v_cvt_pk_bf16_f32 v2, v2, v3
	v_cvt_pk_bf16_f32 v3, v4, v5
	v_cvt_pk_bf16_f32 v4, v8, v9
	v_cvt_pk_bf16_f32 v5, v10, v11
	global_store_dwordx4 v[12:13], v[2:5], off offset:-2560 sc1
	v_pk_mul_f32 v[8:9], v[70:71], s[26:27] op_sel_hi:[1,0]
	v_pk_mul_f32 v[10:11], v[72:73], s[26:27] op_sel_hi:[1,0]
	v_pk_mul_f32 v[2:3], v[66:67], s[26:27] op_sel_hi:[1,0]
	v_pk_mul_f32 v[4:5], v[68:69], s[26:27] op_sel_hi:[1,0]
	v_lshl_add_u64 v[12:13], v[6:7], 0, v[40:41]
	v_cvt_pk_bf16_f32 v2, v2, v3
	v_cvt_pk_bf16_f32 v3, v4, v5
	v_cvt_pk_bf16_f32 v4, v8, v9
	v_cvt_pk_bf16_f32 v5, v10, v11
	global_store_dwordx4 v[12:13], v[2:5], off offset:-2560 sc1
	v_pk_mul_f32 v[8:9], v[78:79], s[26:27] op_sel_hi:[1,0]
	v_pk_mul_f32 v[10:11], v[80:81], s[26:27] op_sel_hi:[1,0]
	v_pk_mul_f32 v[2:3], v[74:75], s[26:27] op_sel_hi:[1,0]
	v_pk_mul_f32 v[4:5], v[76:77], s[26:27] op_sel_hi:[1,0]
	v_lshl_add_u64 v[12:13], v[6:7], 0, v[38:39]
	v_cvt_pk_bf16_f32 v2, v2, v3
	v_cvt_pk_bf16_f32 v3, v4, v5
	v_cvt_pk_bf16_f32 v4, v8, v9
	v_cvt_pk_bf16_f32 v5, v10, v11
	global_store_dwordx4 v[12:13], v[2:5], off offset:-2560 sc1
	v_pk_mul_f32 v[8:9], v[86:87], s[26:27] op_sel_hi:[1,0]
	v_pk_mul_f32 v[10:11], v[88:89], s[26:27] op_sel_hi:[1,0]
	v_pk_mul_f32 v[2:3], v[82:83], s[26:27] op_sel_hi:[1,0]
	v_pk_mul_f32 v[4:5], v[84:85], s[26:27] op_sel_hi:[1,0]
	v_lshl_add_u64 v[12:13], v[6:7], 0, v[36:37]
	v_cvt_pk_bf16_f32 v2, v2, v3
	v_cvt_pk_bf16_f32 v3, v4, v5
	v_cvt_pk_bf16_f32 v4, v8, v9
	v_cvt_pk_bf16_f32 v5, v10, v11
	global_store_dwordx4 v[12:13], v[2:5], off offset:-2560 sc1
	v_pk_mul_f32 v[8:9], v[94:95], s[26:27] op_sel_hi:[1,0]
	v_pk_mul_f32 v[10:11], v[96:97], s[26:27] op_sel_hi:[1,0]
	v_pk_mul_f32 v[2:3], v[90:91], s[26:27] op_sel_hi:[1,0]
	v_pk_mul_f32 v[4:5], v[92:93], s[26:27] op_sel_hi:[1,0]
	v_lshl_add_u64 v[6:7], v[6:7], 0, v[34:35]
	v_cvt_pk_bf16_f32 v2, v2, v3
	v_cvt_pk_bf16_f32 v3, v4, v5
	v_cvt_pk_bf16_f32 v4, v8, v9
	v_cvt_pk_bf16_f32 v5, v10, v11
	global_store_dwordx4 v[6:7], v[2:5], off offset:-2560 sc1

.LBB0_226:
	s_andn2_b64 vcc, exec, s[6:7]
	s_cbranch_vccnz .LBB0_228
	v_mov_b32_e32 v2, v235
	v_mov_b32_e32 v3, v240
	s_add_u32 s6, s74, s44
	s_addc_u32 s7, s75, s45
	v_ashrrev_i32_e32 v3, 31, v2
	v_lshl_add_u64 v[6:7], v[2:3], 1, s[6:7]
	v_lshl_add_u64 v[8:9], v[6:7], 0, v[32:33]
	v_cvt_pk_bf16_f32 v2, v106, v107
	v_cvt_pk_bf16_f32 v3, v108, v109
	v_cvt_pk_bf16_f32 v4, v122, v123
	v_cvt_pk_bf16_f32 v5, v124, v125
	global_store_dwordx4 v[8:9], v[2:5], off sc1
	v_lshl_add_u64 v[8:9], v[6:7], 0, v[30:31]
	s_nop 0
	v_cvt_pk_bf16_f32 v2, v134, v135
	v_cvt_pk_bf16_f32 v3, v136, v137
	v_cvt_pk_bf16_f32 v4, v146, v147
	v_cvt_pk_bf16_f32 v5, v148, v149
	global_store_dwordx4 v[8:9], v[2:5], off sc1
	v_lshl_add_u64 v[8:9], v[6:7], 0, v[28:29]
	s_nop 0
	v_cvt_pk_bf16_f32 v2, v158, v159
	v_cvt_pk_bf16_f32 v3, v160, v161
	v_cvt_pk_bf16_f32 v4, v114, v115
	v_cvt_pk_bf16_f32 v5, v116, v117
	global_store_dwordx4 v[8:9], v[2:5], off sc1
	v_lshl_add_u64 v[8:9], v[6:7], 0, v[26:27]
	s_nop 0
	v_cvt_pk_bf16_f32 v2, v126, v127
	v_cvt_pk_bf16_f32 v3, v128, v129
	v_cvt_pk_bf16_f32 v4, v138, v139
	v_cvt_pk_bf16_f32 v5, v140, v141
	global_store_dwordx4 v[8:9], v[2:5], off sc1
	v_lshl_add_u64 v[8:9], v[6:7], 0, v[24:25]
	s_nop 0
	v_cvt_pk_bf16_f32 v2, v66, v67
	v_cvt_pk_bf16_f32 v3, v68, v69
	v_cvt_pk_bf16_f32 v4, v70, v71
	v_cvt_pk_bf16_f32 v5, v72, v73
	global_store_dwordx4 v[8:9], v[2:5], off sc1
	v_lshl_add_u64 v[8:9], v[6:7], 0, v[22:23]
	s_nop 0
	v_cvt_pk_bf16_f32 v2, v74, v75
	v_cvt_pk_bf16_f32 v3, v76, v77
	v_cvt_pk_bf16_f32 v4, v78, v79
	v_cvt_pk_bf16_f32 v5, v80, v81
	global_store_dwordx4 v[8:9], v[2:5], off sc1
	v_lshl_add_u64 v[8:9], v[6:7], 0, v[20:21]
	v_lshl_add_u64 v[6:7], v[6:7], 0, v[18:19]
	v_cvt_pk_bf16_f32 v2, v82, v83
	v_cvt_pk_bf16_f32 v3, v84, v85
	v_cvt_pk_bf16_f32 v4, v86, v87
	v_cvt_pk_bf16_f32 v5, v88, v89
	global_store_dwordx4 v[8:9], v[2:5], off sc1
	s_nop 1
	v_cvt_pk_bf16_f32 v2, v90, v91
	v_cvt_pk_bf16_f32 v3, v92, v93
	v_cvt_pk_bf16_f32 v4, v94, v95
	v_cvt_pk_bf16_f32 v5, v96, v97
	global_store_dwordx4 v[6:7], v[2:5], off sc1

.LBB0_233:
	s_waitcnt vmcnt(0)
	v_add_u32_e32 v10, 0x400, v224
	global_load_dwordx4 v[6:9], v10, s[14:15] offset:48
	global_load_dwordx4 v[14:17], v10, s[14:15] offset:32
	global_load_dwordx4 v[2:5], v10, s[14:15] offset:16
	s_nop 0
	global_load_dwordx4 v[10:13], v10, s[14:15]
	s_add_u32 s44, s74, s44
	s_addc_u32 s45, s75, s45
	v_ashrrev_i32_e32 v223, 31, v222
	v_lshl_add_u64 v[222:223], v[222:223], 1, s[44:45]
	v_lshl_add_u64 v[242:243], v[222:223], 0, v[32:33]
	v_cvt_pk_bf16_f32 v226, v225, v226
	v_cvt_pk_bf16_f32 v227, v227, v228
	v_cvt_pk_bf16_f32 v228, v229, v230
	v_cvt_pk_bf16_f32 v229, v231, v232
	s_and_b64 vcc, exec, s[6:7]
	global_store_dwordx4 v[242:243], v[226:229], off sc1
	s_cbranch_vccnz .LBB0_235
	s_nop 0
	v_and_b32_e32 v226, 64, v239
	v_xor_b32_e32 v225, 16, v239
	v_add_u32_e32 v226, 64, v226
	v_cmp_lt_i32_e32 vcc, v225, v226
	s_nop 1
	v_cndmask_b32_e32 v225, v239, v225, vcc
	v_lshlrev_b32_e32 v231, 2, v225
	ds_bpermute_b32 v225, v231, v134
	ds_bpermute_b32 v226, v231, v135
	s_waitcnt vmcnt(3) lgkmcnt(1)
	v_mul_f32_e32 v14, v14, v225
	v_cndmask_b32_e64 v14, v14, -v14, s[0:1]
	s_waitcnt vmcnt(1)
	v_fmac_f32_e32 v14, v134, v10
	ds_bpermute_b32 v10, v231, v136
	s_waitcnt lgkmcnt(1)
	v_mul_f32_e32 v15, v15, v226
	v_cndmask_b32_e64 v225, v134, v14, s[2:3]
	v_cndmask_b32_e64 v14, v15, -v15, s[0:1]
	v_fmac_f32_e32 v14, v135, v11
	ds_bpermute_b32 v11, v231, v137
	s_waitcnt lgkmcnt(1)
	v_mul_f32_e32 v10, v16, v10
	v_cndmask_b32_e64 v10, v10, -v10, s[0:1]
	v_fmac_f32_e32 v10, v136, v12
	v_cndmask_b32_e64 v227, v136, v10, s[2:3]
	s_waitcnt lgkmcnt(0)
	v_mul_f32_e32 v10, v17, v11
	ds_bpermute_b32 v11, v231, v146
	v_cndmask_b32_e64 v10, v10, -v10, s[0:1]
	v_fmac_f32_e32 v10, v137, v13
	v_cndmask_b32_e64 v228, v137, v10, s[2:3]
	ds_bpermute_b32 v10, v231, v147
	s_waitcnt lgkmcnt(1)
	v_mul_f32_e32 v6, v6, v11
	v_cndmask_b32_e64 v6, v6, -v6, s[0:1]
	v_fmac_f32_e32 v6, v146, v2
	v_cndmask_b32_e64 v229, v146, v6, s[2:3]
	s_waitcnt lgkmcnt(0)
	v_mul_f32_e32 v2, v7, v10
	v_cndmask_b32_e64 v2, v2, -v2, s[0:1]
	v_fmac_f32_e32 v2, v147, v3
	ds_bpermute_b32 v6, v231, v148
	v_cndmask_b32_e64 v230, v147, v2, s[2:3]
	ds_bpermute_b32 v2, v231, v149
	v_cndmask_b32_e64 v226, v135, v14, s[2:3]
	s_waitcnt lgkmcnt(1)
	v_mul_f32_e32 v3, v8, v6
	v_cndmask_b32_e64 v3, v3, -v3, s[0:1]
	s_waitcnt lgkmcnt(0)
	v_mul_f32_e32 v2, v9, v2
	v_cndmask_b32_e64 v2, v2, -v2, s[0:1]
	v_fmac_f32_e32 v3, v148, v4
	v_fmac_f32_e32 v2, v149, v5
	v_cndmask_b32_e64 v231, v148, v3, s[2:3]
	v_cndmask_b32_e64 v232, v149, v2, s[2:3]
	s_branch .LBB0_236

.LBB0_236:
	s_waitcnt vmcnt(1)
	v_add_u32_e32 v10, 0x800, v224
	global_load_dwordx4 v[6:9], v10, s[14:15] offset:48
	global_load_dwordx4 v[14:17], v10, s[14:15] offset:32
	global_load_dwordx4 v[2:5], v10, s[14:15] offset:16
	s_nop 0
	global_load_dwordx4 v[10:13], v10, s[14:15]
	v_lshl_add_u64 v[242:243], v[222:223], 0, v[30:31]
	v_cvt_pk_bf16_f32 v226, v225, v226
	v_cvt_pk_bf16_f32 v227, v227, v228
	v_cvt_pk_bf16_f32 v228, v229, v230
	v_cvt_pk_bf16_f32 v229, v231, v232
	s_and_b64 vcc, exec, s[6:7]
	global_store_dwordx4 v[242:243], v[226:229], off sc1
	s_cbranch_vccnz .LBB0_238
	s_nop 0
	v_and_b32_e32 v226, 64, v239
	v_xor_b32_e32 v225, 16, v239
	v_add_u32_e32 v226, 64, v226
	v_cmp_lt_i32_e32 vcc, v225, v226
	s_nop 1
	v_cndmask_b32_e32 v225, v239, v225, vcc
	v_lshlrev_b32_e32 v231, 2, v225
	ds_bpermute_b32 v225, v231, v158
	ds_bpermute_b32 v226, v231, v159
	s_waitcnt vmcnt(3) lgkmcnt(1)
	v_mul_f32_e32 v14, v14, v225
	v_cndmask_b32_e64 v14, v14, -v14, s[0:1]
	s_waitcnt vmcnt(1)
	v_fmac_f32_e32 v14, v158, v10
	ds_bpermute_b32 v10, v231, v160
	s_waitcnt lgkmcnt(1)
	v_mul_f32_e32 v15, v15, v226
	v_cndmask_b32_e64 v225, v158, v14, s[2:3]
	v_cndmask_b32_e64 v14, v15, -v15, s[0:1]
	v_fmac_f32_e32 v14, v159, v11
	ds_bpermute_b32 v11, v231, v161
	s_waitcnt lgkmcnt(1)
	v_mul_f32_e32 v10, v16, v10
	v_cndmask_b32_e64 v10, v10, -v10, s[0:1]
	v_fmac_f32_e32 v10, v160, v12
	v_cndmask_b32_e64 v227, v160, v10, s[2:3]
	s_waitcnt lgkmcnt(0)
	v_mul_f32_e32 v10, v17, v11
	ds_bpermute_b32 v11, v231, v114
	v_cndmask_b32_e64 v10, v10, -v10, s[0:1]
	v_fmac_f32_e32 v10, v161, v13
	v_cndmask_b32_e64 v228, v161, v10, s[2:3]
	ds_bpermute_b32 v10, v231, v115
	s_waitcnt lgkmcnt(1)
	v_mul_f32_e32 v6, v6, v11
	v_cndmask_b32_e64 v6, v6, -v6, s[0:1]
	v_fmac_f32_e32 v6, v114, v2
	v_cndmask_b32_e64 v229, v114, v6, s[2:3]
	s_waitcnt lgkmcnt(0)
	v_mul_f32_e32 v2, v7, v10
	v_cndmask_b32_e64 v2, v2, -v2, s[0:1]
	v_fmac_f32_e32 v2, v115, v3
	ds_bpermute_b32 v6, v231, v116
	v_cndmask_b32_e64 v230, v115, v2, s[2:3]
	ds_bpermute_b32 v2, v231, v117
	v_cndmask_b32_e64 v226, v159, v14, s[2:3]
	s_waitcnt lgkmcnt(1)
	v_mul_f32_e32 v3, v8, v6
	v_cndmask_b32_e64 v3, v3, -v3, s[0:1]
	s_waitcnt lgkmcnt(0)
	v_mul_f32_e32 v2, v9, v2
	v_cndmask_b32_e64 v2, v2, -v2, s[0:1]
	v_fmac_f32_e32 v3, v116, v4
	v_fmac_f32_e32 v2, v117, v5
	v_cndmask_b32_e64 v231, v116, v3, s[2:3]
	v_cndmask_b32_e64 v232, v117, v2, s[2:3]
	s_branch .LBB0_239

.LBB0_239:
	s_waitcnt vmcnt(1)
	v_add_u32_e32 v10, 0xc00, v224
	global_load_dwordx4 v[6:9], v10, s[14:15] offset:48
	global_load_dwordx4 v[14:17], v10, s[14:15] offset:32
	global_load_dwordx4 v[2:5], v10, s[14:15] offset:16
	s_nop 0
	global_load_dwordx4 v[10:13], v10, s[14:15]
	v_lshl_add_u64 v[242:243], v[222:223], 0, v[28:29]
	v_cvt_pk_bf16_f32 v226, v225, v226
	v_cvt_pk_bf16_f32 v227, v227, v228
	v_cvt_pk_bf16_f32 v228, v229, v230
	v_cvt_pk_bf16_f32 v229, v231, v232
	s_and_b64 vcc, exec, s[6:7]
	global_store_dwordx4 v[242:243], v[226:229], off sc1
	s_cbranch_vccnz .LBB0_241
	s_nop 0
	v_and_b32_e32 v226, 64, v239
	v_xor_b32_e32 v225, 16, v239
	v_add_u32_e32 v226, 64, v226
	v_cmp_lt_i32_e32 vcc, v225, v226
	s_nop 1
	v_cndmask_b32_e32 v225, v239, v225, vcc
	v_lshlrev_b32_e32 v231, 2, v225
	ds_bpermute_b32 v225, v231, v126
	ds_bpermute_b32 v226, v231, v127
	s_waitcnt vmcnt(3) lgkmcnt(1)
	v_mul_f32_e32 v14, v14, v225
	v_cndmask_b32_e64 v14, v14, -v14, s[0:1]
	s_waitcnt vmcnt(1)
	v_fmac_f32_e32 v14, v126, v10
	ds_bpermute_b32 v10, v231, v128
	s_waitcnt lgkmcnt(1)
	v_mul_f32_e32 v15, v15, v226
	v_cndmask_b32_e64 v225, v126, v14, s[2:3]
	v_cndmask_b32_e64 v14, v15, -v15, s[0:1]
	v_fmac_f32_e32 v14, v127, v11
	ds_bpermute_b32 v11, v231, v129
	s_waitcnt lgkmcnt(1)
	v_mul_f32_e32 v10, v16, v10
	v_cndmask_b32_e64 v10, v10, -v10, s[0:1]
	v_fmac_f32_e32 v10, v128, v12
	v_cndmask_b32_e64 v227, v128, v10, s[2:3]
	s_waitcnt lgkmcnt(0)
	v_mul_f32_e32 v10, v17, v11
	ds_bpermute_b32 v11, v231, v138
	v_cndmask_b32_e64 v10, v10, -v10, s[0:1]
	v_fmac_f32_e32 v10, v129, v13
	v_cndmask_b32_e64 v228, v129, v10, s[2:3]
	ds_bpermute_b32 v10, v231, v139
	s_waitcnt lgkmcnt(1)
	v_mul_f32_e32 v6, v6, v11
	v_cndmask_b32_e64 v6, v6, -v6, s[0:1]
	v_fmac_f32_e32 v6, v138, v2
	v_cndmask_b32_e64 v229, v138, v6, s[2:3]
	s_waitcnt lgkmcnt(0)
	v_mul_f32_e32 v2, v7, v10
	v_cndmask_b32_e64 v2, v2, -v2, s[0:1]
	v_fmac_f32_e32 v2, v139, v3
	ds_bpermute_b32 v6, v231, v140
	v_cndmask_b32_e64 v230, v139, v2, s[2:3]
	ds_bpermute_b32 v2, v231, v141
	v_cndmask_b32_e64 v226, v127, v14, s[2:3]
	s_waitcnt lgkmcnt(1)
	v_mul_f32_e32 v3, v8, v6
	v_cndmask_b32_e64 v3, v3, -v3, s[0:1]
	s_waitcnt lgkmcnt(0)
	v_mul_f32_e32 v2, v9, v2
	v_cndmask_b32_e64 v2, v2, -v2, s[0:1]
	v_fmac_f32_e32 v3, v140, v4
	v_fmac_f32_e32 v2, v141, v5
	v_cndmask_b32_e64 v231, v140, v3, s[2:3]
	v_cndmask_b32_e64 v232, v141, v2, s[2:3]
	s_branch .LBB0_242

.LBB0_242:
	s_waitcnt vmcnt(1)
	v_add_u32_e32 v10, 0x2000, v224
	global_load_dwordx4 v[6:9], v10, s[14:15] offset:48
	global_load_dwordx4 v[14:17], v10, s[14:15] offset:32
	global_load_dwordx4 v[2:5], v10, s[14:15] offset:16
	s_nop 0
	global_load_dwordx4 v[10:13], v10, s[14:15]
	v_lshl_add_u64 v[242:243], v[222:223], 0, v[26:27]
	v_cvt_pk_bf16_f32 v226, v225, v226
	v_cvt_pk_bf16_f32 v227, v227, v228
	v_cvt_pk_bf16_f32 v228, v229, v230
	v_cvt_pk_bf16_f32 v229, v231, v232
	s_and_b64 vcc, exec, s[6:7]
	global_store_dwordx4 v[242:243], v[226:229], off sc1
	s_cbranch_vccnz .LBB0_244
	s_nop 0
	v_and_b32_e32 v226, 64, v239
	v_xor_b32_e32 v225, 16, v239
	v_add_u32_e32 v226, 64, v226
	v_cmp_lt_i32_e32 vcc, v225, v226
	s_nop 1
	v_cndmask_b32_e32 v225, v239, v225, vcc
	v_lshlrev_b32_e32 v231, 2, v225
	ds_bpermute_b32 v225, v231, v66
	ds_bpermute_b32 v226, v231, v67
	s_waitcnt vmcnt(3) lgkmcnt(1)
	v_mul_f32_e32 v14, v14, v225
	v_cndmask_b32_e64 v14, v14, -v14, s[0:1]
	s_waitcnt vmcnt(1)
	v_fmac_f32_e32 v14, v66, v10
	ds_bpermute_b32 v10, v231, v68
	s_waitcnt lgkmcnt(1)
	v_mul_f32_e32 v15, v15, v226
	v_cndmask_b32_e64 v225, v66, v14, s[2:3]
	v_cndmask_b32_e64 v14, v15, -v15, s[0:1]
	v_fmac_f32_e32 v14, v67, v11
	ds_bpermute_b32 v11, v231, v69
	s_waitcnt lgkmcnt(1)
	v_mul_f32_e32 v10, v16, v10
	v_cndmask_b32_e64 v10, v10, -v10, s[0:1]
	v_fmac_f32_e32 v10, v68, v12
	v_cndmask_b32_e64 v227, v68, v10, s[2:3]
	s_waitcnt lgkmcnt(0)
	v_mul_f32_e32 v10, v17, v11
	ds_bpermute_b32 v11, v231, v70
	v_cndmask_b32_e64 v10, v10, -v10, s[0:1]
	v_fmac_f32_e32 v10, v69, v13
	v_cndmask_b32_e64 v228, v69, v10, s[2:3]
	ds_bpermute_b32 v10, v231, v71
	s_waitcnt lgkmcnt(1)
	v_mul_f32_e32 v6, v6, v11
	v_cndmask_b32_e64 v6, v6, -v6, s[0:1]
	v_fmac_f32_e32 v6, v70, v2
	v_cndmask_b32_e64 v229, v70, v6, s[2:3]
	s_waitcnt lgkmcnt(0)
	v_mul_f32_e32 v2, v7, v10
	v_cndmask_b32_e64 v2, v2, -v2, s[0:1]
	v_fmac_f32_e32 v2, v71, v3
	ds_bpermute_b32 v6, v231, v72
	v_cndmask_b32_e64 v230, v71, v2, s[2:3]
	ds_bpermute_b32 v2, v231, v73
	v_cndmask_b32_e64 v226, v67, v14, s[2:3]
	s_waitcnt lgkmcnt(1)
	v_mul_f32_e32 v3, v8, v6
	v_cndmask_b32_e64 v3, v3, -v3, s[0:1]
	s_waitcnt lgkmcnt(0)
	v_mul_f32_e32 v2, v9, v2
	v_cndmask_b32_e64 v2, v2, -v2, s[0:1]
	v_fmac_f32_e32 v3, v72, v4
	v_fmac_f32_e32 v2, v73, v5
	v_cndmask_b32_e64 v231, v72, v3, s[2:3]
	v_cndmask_b32_e64 v232, v73, v2, s[2:3]
	s_branch .LBB0_245

.LBB0_245:
	s_waitcnt vmcnt(1)
	v_add_u32_e32 v10, 0x2400, v224
	global_load_dwordx4 v[6:9], v10, s[14:15] offset:48
	global_load_dwordx4 v[14:17], v10, s[14:15] offset:32
	global_load_dwordx4 v[2:5], v10, s[14:15] offset:16
	s_nop 0
	global_load_dwordx4 v[10:13], v10, s[14:15]
	v_lshl_add_u64 v[242:243], v[222:223], 0, v[24:25]
	v_cvt_pk_bf16_f32 v226, v225, v226
	v_cvt_pk_bf16_f32 v227, v227, v228
	v_cvt_pk_bf16_f32 v228, v229, v230
	v_cvt_pk_bf16_f32 v229, v231, v232
	s_and_b64 vcc, exec, s[6:7]
	global_store_dwordx4 v[242:243], v[226:229], off sc1
	s_cbranch_vccnz .LBB0_247
	s_nop 0
	v_and_b32_e32 v226, 64, v239
	v_xor_b32_e32 v225, 16, v239
	v_add_u32_e32 v226, 64, v226
	v_cmp_lt_i32_e32 vcc, v225, v226
	s_nop 1
	v_cndmask_b32_e32 v225, v239, v225, vcc
	v_lshlrev_b32_e32 v231, 2, v225
	ds_bpermute_b32 v225, v231, v74
	ds_bpermute_b32 v226, v231, v75
	s_waitcnt vmcnt(3) lgkmcnt(1)
	v_mul_f32_e32 v14, v14, v225
	v_cndmask_b32_e64 v14, v14, -v14, s[0:1]
	s_waitcnt vmcnt(1)
	v_fmac_f32_e32 v14, v74, v10
	ds_bpermute_b32 v10, v231, v76
	s_waitcnt lgkmcnt(1)
	v_mul_f32_e32 v15, v15, v226
	v_cndmask_b32_e64 v225, v74, v14, s[2:3]
	v_cndmask_b32_e64 v14, v15, -v15, s[0:1]
	v_fmac_f32_e32 v14, v75, v11
	ds_bpermute_b32 v11, v231, v77
	s_waitcnt lgkmcnt(1)
	v_mul_f32_e32 v10, v16, v10
	v_cndmask_b32_e64 v10, v10, -v10, s[0:1]
	v_fmac_f32_e32 v10, v76, v12
	v_cndmask_b32_e64 v227, v76, v10, s[2:3]
	s_waitcnt lgkmcnt(0)
	v_mul_f32_e32 v10, v17, v11
	ds_bpermute_b32 v11, v231, v78
	v_cndmask_b32_e64 v10, v10, -v10, s[0:1]
	v_fmac_f32_e32 v10, v77, v13
	v_cndmask_b32_e64 v228, v77, v10, s[2:3]
	ds_bpermute_b32 v10, v231, v79
	s_waitcnt lgkmcnt(1)
	v_mul_f32_e32 v6, v6, v11
	v_cndmask_b32_e64 v6, v6, -v6, s[0:1]
	v_fmac_f32_e32 v6, v78, v2
	v_cndmask_b32_e64 v229, v78, v6, s[2:3]
	s_waitcnt lgkmcnt(0)
	v_mul_f32_e32 v2, v7, v10
	v_cndmask_b32_e64 v2, v2, -v2, s[0:1]
	v_fmac_f32_e32 v2, v79, v3
	ds_bpermute_b32 v6, v231, v80
	v_cndmask_b32_e64 v230, v79, v2, s[2:3]
	ds_bpermute_b32 v2, v231, v81
	v_cndmask_b32_e64 v226, v75, v14, s[2:3]
	s_waitcnt lgkmcnt(1)
	v_mul_f32_e32 v3, v8, v6
	v_cndmask_b32_e64 v3, v3, -v3, s[0:1]
	s_waitcnt lgkmcnt(0)
	v_mul_f32_e32 v2, v9, v2
	v_cndmask_b32_e64 v2, v2, -v2, s[0:1]
	v_fmac_f32_e32 v3, v80, v4
	v_fmac_f32_e32 v2, v81, v5
	v_cndmask_b32_e64 v231, v80, v3, s[2:3]
	v_cndmask_b32_e64 v232, v81, v2, s[2:3]
	s_branch .LBB0_248

.LBB0_248:
	s_waitcnt vmcnt(1)
	v_add_u32_e32 v10, 0x2800, v224
	global_load_dwordx4 v[6:9], v10, s[14:15] offset:48
	global_load_dwordx4 v[14:17], v10, s[14:15] offset:32
	global_load_dwordx4 v[2:5], v10, s[14:15] offset:16
	s_nop 0
	global_load_dwordx4 v[10:13], v10, s[14:15]
	v_lshl_add_u64 v[242:243], v[222:223], 0, v[22:23]
	v_cvt_pk_bf16_f32 v226, v225, v226
	v_cvt_pk_bf16_f32 v227, v227, v228
	v_cvt_pk_bf16_f32 v228, v229, v230
	v_cvt_pk_bf16_f32 v229, v231, v232
	s_and_b64 vcc, exec, s[6:7]
	global_store_dwordx4 v[242:243], v[226:229], off sc1
	s_cbranch_vccnz .LBB0_250
	s_nop 0
	v_and_b32_e32 v226, 64, v239
	v_xor_b32_e32 v225, 16, v239
	v_add_u32_e32 v226, 64, v226
	v_cmp_lt_i32_e32 vcc, v225, v226
	s_nop 1
	v_cndmask_b32_e32 v225, v239, v225, vcc
	v_lshlrev_b32_e32 v231, 2, v225
	ds_bpermute_b32 v225, v231, v82
	ds_bpermute_b32 v226, v231, v83
	s_waitcnt vmcnt(3) lgkmcnt(1)
	v_mul_f32_e32 v14, v14, v225
	v_cndmask_b32_e64 v14, v14, -v14, s[0:1]
	s_waitcnt vmcnt(1)
	v_fmac_f32_e32 v14, v82, v10
	ds_bpermute_b32 v10, v231, v84
	s_waitcnt lgkmcnt(1)
	v_mul_f32_e32 v15, v15, v226
	v_cndmask_b32_e64 v225, v82, v14, s[2:3]
	v_cndmask_b32_e64 v14, v15, -v15, s[0:1]
	v_fmac_f32_e32 v14, v83, v11
	ds_bpermute_b32 v11, v231, v85
	s_waitcnt lgkmcnt(1)
	v_mul_f32_e32 v10, v16, v10
	v_cndmask_b32_e64 v10, v10, -v10, s[0:1]
	v_fmac_f32_e32 v10, v84, v12
	v_cndmask_b32_e64 v227, v84, v10, s[2:3]
	s_waitcnt lgkmcnt(0)
	v_mul_f32_e32 v10, v17, v11
	ds_bpermute_b32 v11, v231, v86
	v_cndmask_b32_e64 v10, v10, -v10, s[0:1]
	v_fmac_f32_e32 v10, v85, v13
	v_cndmask_b32_e64 v228, v85, v10, s[2:3]
	ds_bpermute_b32 v10, v231, v87
	s_waitcnt lgkmcnt(1)
	v_mul_f32_e32 v6, v6, v11
	v_cndmask_b32_e64 v6, v6, -v6, s[0:1]
	v_fmac_f32_e32 v6, v86, v2
	v_cndmask_b32_e64 v229, v86, v6, s[2:3]
	s_waitcnt lgkmcnt(0)
	v_mul_f32_e32 v2, v7, v10
	v_cndmask_b32_e64 v2, v2, -v2, s[0:1]
	v_fmac_f32_e32 v2, v87, v3
	ds_bpermute_b32 v6, v231, v88
	v_cndmask_b32_e64 v230, v87, v2, s[2:3]
	ds_bpermute_b32 v2, v231, v89
	v_cndmask_b32_e64 v226, v83, v14, s[2:3]
	s_waitcnt lgkmcnt(1)
	v_mul_f32_e32 v3, v8, v6
	v_cndmask_b32_e64 v3, v3, -v3, s[0:1]
	s_waitcnt lgkmcnt(0)
	v_mul_f32_e32 v2, v9, v2
	v_cndmask_b32_e64 v2, v2, -v2, s[0:1]
	v_fmac_f32_e32 v3, v88, v4
	v_fmac_f32_e32 v2, v89, v5
	v_cndmask_b32_e64 v231, v88, v3, s[2:3]
	v_cndmask_b32_e64 v232, v89, v2, s[2:3]
	s_branch .LBB0_251

.LBB0_251:
	s_waitcnt vmcnt(1)
	v_add_u32_e32 v10, 0x2c00, v224
	global_load_dwordx4 v[6:9], v10, s[14:15] offset:48
	global_load_dwordx4 v[14:17], v10, s[14:15] offset:32
	global_load_dwordx4 v[2:5], v10, s[14:15] offset:16
	s_nop 0
	global_load_dwordx4 v[10:13], v10, s[14:15]
	v_lshl_add_u64 v[242:243], v[222:223], 0, v[20:21]
	v_cvt_pk_bf16_f32 v224, v225, v226
	v_cvt_pk_bf16_f32 v225, v227, v228
	v_cvt_pk_bf16_f32 v226, v229, v230
	v_cvt_pk_bf16_f32 v227, v231, v232
	s_and_b64 vcc, exec, s[6:7]
	global_store_dwordx4 v[242:243], v[224:227], off sc1
	s_cbranch_vccnz .LBB0_253
	s_nop 0
	v_and_b32_e32 v225, 64, v239
	v_xor_b32_e32 v224, 16, v239
	v_add_u32_e32 v225, 64, v225
	v_cmp_lt_i32_e32 vcc, v224, v225
	s_nop 1
	v_cndmask_b32_e32 v224, v239, v224, vcc
	v_lshlrev_b32_e32 v224, 2, v224
	ds_bpermute_b32 v225, v224, v90
	ds_bpermute_b32 v226, v224, v91
	s_waitcnt vmcnt(3) lgkmcnt(1)
	v_mul_f32_e32 v14, v14, v225
	v_cndmask_b32_e64 v14, v14, -v14, s[0:1]
	s_waitcnt vmcnt(1)
	v_fmac_f32_e32 v14, v90, v10
	s_waitcnt lgkmcnt(0)
	v_mul_f32_e32 v15, v15, v226
	v_cndmask_b32_e64 v10, v90, v14, s[2:3]
	ds_bpermute_b32 v14, v224, v92
	v_cndmask_b32_e64 v15, v15, -v15, s[0:1]
	v_fmac_f32_e32 v15, v91, v11
	v_cndmask_b32_e64 v11, v91, v15, s[2:3]
	ds_bpermute_b32 v15, v224, v93
	s_waitcnt lgkmcnt(1)
	v_mul_f32_e32 v14, v16, v14
	v_cndmask_b32_e64 v14, v14, -v14, s[0:1]
	v_fmac_f32_e32 v14, v92, v12
	v_cndmask_b32_e64 v12, v92, v14, s[2:3]
	s_waitcnt lgkmcnt(0)
	v_mul_f32_e32 v14, v17, v15
	ds_bpermute_b32 v15, v224, v94
	v_cndmask_b32_e64 v14, v14, -v14, s[0:1]
	v_fmac_f32_e32 v14, v93, v13
	v_cndmask_b32_e64 v13, v93, v14, s[2:3]
	ds_bpermute_b32 v14, v224, v95
	s_waitcnt lgkmcnt(1)
	v_mul_f32_e32 v6, v6, v15
	v_cndmask_b32_e64 v6, v6, -v6, s[0:1]
	v_fmac_f32_e32 v6, v94, v2
	v_cndmask_b32_e64 v2, v94, v6, s[2:3]
	s_waitcnt lgkmcnt(0)
	v_mul_f32_e32 v6, v7, v14
	v_cndmask_b32_e64 v6, v6, -v6, s[0:1]
	v_fmac_f32_e32 v6, v95, v3
	ds_bpermute_b32 v7, v224, v96
	v_cndmask_b32_e64 v3, v95, v6, s[2:3]
	ds_bpermute_b32 v6, v224, v97
	s_waitcnt lgkmcnt(1)
	v_mul_f32_e32 v7, v8, v7
	v_cndmask_b32_e64 v7, v7, -v7, s[0:1]
	s_waitcnt lgkmcnt(0)
	v_mul_f32_e32 v6, v9, v6
	v_cndmask_b32_e64 v6, v6, -v6, s[0:1]
	v_fmac_f32_e32 v7, v96, v4
	v_fmac_f32_e32 v6, v97, v5
	v_cndmask_b32_e64 v4, v96, v7, s[2:3]
	v_cndmask_b32_e64 v5, v97, v6, s[2:3]
	s_branch .LBB0_254

.LBB0_254:
	v_lshl_add_u64 v[14:15], v[222:223], 0, v[18:19]
	v_cvt_pk_bf16_f32 v6, v10, v11
	v_cvt_pk_bf16_f32 v7, v12, v13
	v_cvt_pk_bf16_f32 v8, v2, v3
	v_cvt_pk_bf16_f32 v9, v4, v5
	global_store_dwordx4 v[14:15], v[6:9], off sc1

.LBB0_263:
	s_waitcnt vmcnt(0)
	v_add_u32_e32 v10, 0x400, v241
	global_load_dwordx4 v[6:9], v10, s[14:15] offset:48
	global_load_dwordx4 v[14:17], v10, s[14:15] offset:32
	global_load_dwordx4 v[2:5], v10, s[14:15] offset:16
	s_nop 0
	global_load_dwordx4 v[10:13], v10, s[14:15]
	s_lshl_b32 s42, s42, 8
	s_ashr_i32 s43, s42, 31
	s_lshl_b64 s[42:43], s[42:43], 1
	s_add_u32 s44, s70, s42
	s_addc_u32 s45, s71, s43
	v_ashrrev_i32_e32 v215, 31, v214
	s_add_u32 s42, s72, s42
	v_lshlrev_b64 v[214:215], 1, v[214:215]
	s_addc_u32 s43, s73, s43
	v_lshl_add_u64 v[216:217], s[44:45], 0, v[214:215]
	v_lshlrev_b64 v[250:251], 1, v[228:229]
	v_lshl_add_u64 v[214:215], s[42:43], 0, v[214:215]
	v_lshl_add_u64 v[252:253], v[216:217], 0, v[250:251]
	v_cvt_pk_bf16_f32 v218, v218, v219
	v_cvt_pk_bf16_f32 v219, v220, v221
	v_cvt_pk_bf16_f32 v220, v230, v231
	v_cvt_pk_bf16_f32 v221, v232, v233
	global_store_dwordx4 v[252:253], v[218:221], off sc1
	v_lshl_add_u64 v[230:231], v[214:215], 0, v[250:251]
	s_and_b64 vcc, exec, s[6:7]
	v_cvt_pk_bf16_f32 v218, v242, v243
	v_cvt_pk_bf16_f32 v219, v244, v245
	v_cvt_pk_bf16_f32 v220, v246, v247
	v_cvt_pk_bf16_f32 v221, v248, v249
	global_store_dwordx4 v[230:231], v[218:221], off sc1
	v_pk_mul_f32 v[230:231], v[146:147], s[26:27] op_sel_hi:[1,0]
	v_pk_mul_f32 v[232:233], v[148:149], s[26:27] op_sel_hi:[1,0]
	v_pk_mul_f32 v[218:219], v[134:135], s[26:27] op_sel_hi:[1,0]
	v_pk_mul_f32 v[220:221], v[136:137], s[26:27] op_sel_hi:[1,0]
	s_cbranch_vccnz .LBB0_265
	v_and_b32_e32 v243, 64, v239
	v_xor_b32_e32 v242, 16, v239
	v_add_u32_e32 v243, 64, v243
	v_cmp_lt_i32_e32 vcc, v242, v243
	s_nop 1
	v_cndmask_b32_e32 v242, v239, v242, vcc
	v_lshlrev_b32_e32 v248, 2, v242
	ds_bpermute_b32 v242, v248, v218
	ds_bpermute_b32 v243, v248, v219
	s_waitcnt vmcnt(4) lgkmcnt(1)
	v_mul_f32_e32 v14, v14, v242
	v_cndmask_b32_e64 v14, v14, -v14, s[0:1]
	s_waitcnt vmcnt(2)
	v_fmac_f32_e32 v14, v218, v10
	ds_bpermute_b32 v10, v248, v220
	s_waitcnt lgkmcnt(1)
	v_mul_f32_e32 v15, v15, v243
	v_cndmask_b32_e64 v242, v218, v14, s[2:3]
	v_cndmask_b32_e64 v14, v15, -v15, s[0:1]
	v_fmac_f32_e32 v14, v219, v11
	ds_bpermute_b32 v11, v248, v221
	s_waitcnt lgkmcnt(1)
	v_mul_f32_e32 v10, v16, v10
	v_cndmask_b32_e64 v10, v10, -v10, s[0:1]
	v_fmac_f32_e32 v10, v220, v12
	v_cndmask_b32_e64 v244, v220, v10, s[2:3]
	s_waitcnt lgkmcnt(0)
	v_mul_f32_e32 v10, v17, v11
	ds_bpermute_b32 v11, v248, v230
	v_cndmask_b32_e64 v10, v10, -v10, s[0:1]
	v_fmac_f32_e32 v10, v221, v13
	v_cndmask_b32_e64 v245, v221, v10, s[2:3]
	ds_bpermute_b32 v10, v248, v231
	s_waitcnt lgkmcnt(1)
	v_mul_f32_e32 v6, v6, v11
	v_cndmask_b32_e64 v6, v6, -v6, s[0:1]
	v_fmac_f32_e32 v6, v230, v2
	v_cndmask_b32_e64 v246, v230, v6, s[2:3]
	s_waitcnt lgkmcnt(0)
	v_mul_f32_e32 v2, v7, v10
	v_cndmask_b32_e64 v2, v2, -v2, s[0:1]
	v_fmac_f32_e32 v2, v231, v3
	ds_bpermute_b32 v6, v248, v232
	v_cndmask_b32_e64 v247, v231, v2, s[2:3]
	ds_bpermute_b32 v2, v248, v233
	v_cndmask_b32_e64 v243, v219, v14, s[2:3]
	s_waitcnt lgkmcnt(1)
	v_mul_f32_e32 v3, v8, v6
	v_cndmask_b32_e64 v3, v3, -v3, s[0:1]
	s_waitcnt lgkmcnt(0)
	v_mul_f32_e32 v2, v9, v2
	v_cndmask_b32_e64 v2, v2, -v2, s[0:1]
	v_fmac_f32_e32 v3, v232, v4
	v_fmac_f32_e32 v2, v233, v5
	v_cndmask_b32_e64 v248, v232, v3, s[2:3]
	v_cndmask_b32_e64 v249, v233, v2, s[2:3]
	s_branch .LBB0_266

.LBB0_266:
	s_waitcnt vmcnt(2)
	v_add_u32_e32 v10, 0x800, v241
	global_load_dwordx4 v[6:9], v10, s[14:15] offset:48
	global_load_dwordx4 v[14:17], v10, s[14:15] offset:32
	global_load_dwordx4 v[2:5], v10, s[14:15] offset:16
	s_nop 0
	global_load_dwordx4 v[10:13], v10, s[14:15]
	v_lshlrev_b64 v[250:251], 1, v[226:227]
	v_lshl_add_u64 v[252:253], v[216:217], 0, v[250:251]
	v_cvt_pk_bf16_f32 v218, v218, v219
	v_cvt_pk_bf16_f32 v219, v220, v221
	v_cvt_pk_bf16_f32 v220, v230, v231
	v_cvt_pk_bf16_f32 v221, v232, v233
	global_store_dwordx4 v[252:253], v[218:221], off sc1
	v_lshl_add_u64 v[230:231], v[214:215], 0, v[250:251]
	s_and_b64 vcc, exec, s[6:7]
	v_cvt_pk_bf16_f32 v218, v242, v243
	v_cvt_pk_bf16_f32 v219, v244, v245
	v_cvt_pk_bf16_f32 v220, v246, v247
	v_cvt_pk_bf16_f32 v221, v248, v249
	global_store_dwordx4 v[230:231], v[218:221], off sc1
	v_pk_mul_f32 v[230:231], v[114:115], s[26:27] op_sel_hi:[1,0]
	v_pk_mul_f32 v[232:233], v[116:117], s[26:27] op_sel_hi:[1,0]
	v_pk_mul_f32 v[218:219], v[158:159], s[26:27] op_sel_hi:[1,0]
	v_pk_mul_f32 v[220:221], v[160:161], s[26:27] op_sel_hi:[1,0]
	s_cbranch_vccnz .LBB0_268
	v_and_b32_e32 v243, 64, v239
	v_xor_b32_e32 v242, 16, v239
	v_add_u32_e32 v243, 64, v243
	v_cmp_lt_i32_e32 vcc, v242, v243
	s_nop 1
	v_cndmask_b32_e32 v242, v239, v242, vcc
	v_lshlrev_b32_e32 v248, 2, v242
	ds_bpermute_b32 v242, v248, v218
	ds_bpermute_b32 v243, v248, v219
	s_waitcnt vmcnt(4) lgkmcnt(1)
	v_mul_f32_e32 v14, v14, v242
	v_cndmask_b32_e64 v14, v14, -v14, s[0:1]
	s_waitcnt vmcnt(2)
	v_fmac_f32_e32 v14, v218, v10
	ds_bpermute_b32 v10, v248, v220
	s_waitcnt lgkmcnt(1)
	v_mul_f32_e32 v15, v15, v243
	v_cndmask_b32_e64 v242, v218, v14, s[2:3]
	v_cndmask_b32_e64 v14, v15, -v15, s[0:1]
	v_fmac_f32_e32 v14, v219, v11
	ds_bpermute_b32 v11, v248, v221
	s_waitcnt lgkmcnt(1)
	v_mul_f32_e32 v10, v16, v10
	v_cndmask_b32_e64 v10, v10, -v10, s[0:1]
	v_fmac_f32_e32 v10, v220, v12
	v_cndmask_b32_e64 v244, v220, v10, s[2:3]
	s_waitcnt lgkmcnt(0)
	v_mul_f32_e32 v10, v17, v11
	ds_bpermute_b32 v11, v248, v230
	v_cndmask_b32_e64 v10, v10, -v10, s[0:1]
	v_fmac_f32_e32 v10, v221, v13
	v_cndmask_b32_e64 v245, v221, v10, s[2:3]
	ds_bpermute_b32 v10, v248, v231
	s_waitcnt lgkmcnt(1)
	v_mul_f32_e32 v6, v6, v11
	v_cndmask_b32_e64 v6, v6, -v6, s[0:1]
	v_fmac_f32_e32 v6, v230, v2
	v_cndmask_b32_e64 v246, v230, v6, s[2:3]
	s_waitcnt lgkmcnt(0)
	v_mul_f32_e32 v2, v7, v10
	v_cndmask_b32_e64 v2, v2, -v2, s[0:1]
	v_fmac_f32_e32 v2, v231, v3
	ds_bpermute_b32 v6, v248, v232
	v_cndmask_b32_e64 v247, v231, v2, s[2:3]
	ds_bpermute_b32 v2, v248, v233
	v_cndmask_b32_e64 v243, v219, v14, s[2:3]
	s_waitcnt lgkmcnt(1)
	v_mul_f32_e32 v3, v8, v6
	v_cndmask_b32_e64 v3, v3, -v3, s[0:1]
	s_waitcnt lgkmcnt(0)
	v_mul_f32_e32 v2, v9, v2
	v_cndmask_b32_e64 v2, v2, -v2, s[0:1]
	v_fmac_f32_e32 v3, v232, v4
	v_fmac_f32_e32 v2, v233, v5
	v_cndmask_b32_e64 v248, v232, v3, s[2:3]
	v_cndmask_b32_e64 v249, v233, v2, s[2:3]
	s_branch .LBB0_269

.LBB0_269:
	s_waitcnt vmcnt(2)
	v_add_u32_e32 v10, 0xc00, v241
	global_load_dwordx4 v[6:9], v10, s[14:15] offset:48
	global_load_dwordx4 v[14:17], v10, s[14:15] offset:32
	global_load_dwordx4 v[2:5], v10, s[14:15] offset:16
	s_nop 0
	global_load_dwordx4 v[10:13], v10, s[14:15]
	v_lshlrev_b64 v[250:251], 1, v[224:225]
	v_lshl_add_u64 v[252:253], v[216:217], 0, v[250:251]
	v_cvt_pk_bf16_f32 v218, v218, v219
	v_cvt_pk_bf16_f32 v219, v220, v221
	v_cvt_pk_bf16_f32 v220, v230, v231
	v_cvt_pk_bf16_f32 v221, v232, v233
	global_store_dwordx4 v[252:253], v[218:221], off sc1
	v_lshl_add_u64 v[230:231], v[214:215], 0, v[250:251]
	s_and_b64 vcc, exec, s[6:7]
	v_cvt_pk_bf16_f32 v218, v242, v243
	v_cvt_pk_bf16_f32 v219, v244, v245
	v_cvt_pk_bf16_f32 v220, v246, v247
	v_cvt_pk_bf16_f32 v221, v248, v249
	global_store_dwordx4 v[230:231], v[218:221], off sc1
	v_pk_mul_f32 v[230:231], v[138:139], s[26:27] op_sel_hi:[1,0]
	v_pk_mul_f32 v[232:233], v[140:141], s[26:27] op_sel_hi:[1,0]
	v_pk_mul_f32 v[218:219], v[126:127], s[26:27] op_sel_hi:[1,0]
	v_pk_mul_f32 v[220:221], v[128:129], s[26:27] op_sel_hi:[1,0]
	s_cbranch_vccnz .LBB0_271
	v_and_b32_e32 v243, 64, v239
	v_xor_b32_e32 v242, 16, v239
	v_add_u32_e32 v243, 64, v243
	v_cmp_lt_i32_e32 vcc, v242, v243
	s_nop 1
	v_cndmask_b32_e32 v242, v239, v242, vcc
	v_lshlrev_b32_e32 v248, 2, v242
	ds_bpermute_b32 v242, v248, v218
	ds_bpermute_b32 v243, v248, v219
	s_waitcnt vmcnt(4) lgkmcnt(1)
	v_mul_f32_e32 v14, v14, v242
	v_cndmask_b32_e64 v14, v14, -v14, s[0:1]
	s_waitcnt vmcnt(2)
	v_fmac_f32_e32 v14, v218, v10
	ds_bpermute_b32 v10, v248, v220
	s_waitcnt lgkmcnt(1)
	v_mul_f32_e32 v15, v15, v243
	v_cndmask_b32_e64 v242, v218, v14, s[2:3]
	v_cndmask_b32_e64 v14, v15, -v15, s[0:1]
	v_fmac_f32_e32 v14, v219, v11
	ds_bpermute_b32 v11, v248, v221
	s_waitcnt lgkmcnt(1)
	v_mul_f32_e32 v10, v16, v10
	v_cndmask_b32_e64 v10, v10, -v10, s[0:1]
	v_fmac_f32_e32 v10, v220, v12
	v_cndmask_b32_e64 v244, v220, v10, s[2:3]
	s_waitcnt lgkmcnt(0)
	v_mul_f32_e32 v10, v17, v11
	ds_bpermute_b32 v11, v248, v230
	v_cndmask_b32_e64 v10, v10, -v10, s[0:1]
	v_fmac_f32_e32 v10, v221, v13
	v_cndmask_b32_e64 v245, v221, v10, s[2:3]
	ds_bpermute_b32 v10, v248, v231
	s_waitcnt lgkmcnt(1)
	v_mul_f32_e32 v6, v6, v11
	v_cndmask_b32_e64 v6, v6, -v6, s[0:1]
	v_fmac_f32_e32 v6, v230, v2
	v_cndmask_b32_e64 v246, v230, v6, s[2:3]
	s_waitcnt lgkmcnt(0)
	v_mul_f32_e32 v2, v7, v10
	v_cndmask_b32_e64 v2, v2, -v2, s[0:1]
	v_fmac_f32_e32 v2, v231, v3
	ds_bpermute_b32 v6, v248, v232
	v_cndmask_b32_e64 v247, v231, v2, s[2:3]
	ds_bpermute_b32 v2, v248, v233
	v_cndmask_b32_e64 v243, v219, v14, s[2:3]
	s_waitcnt lgkmcnt(1)
	v_mul_f32_e32 v3, v8, v6
	v_cndmask_b32_e64 v3, v3, -v3, s[0:1]
	s_waitcnt lgkmcnt(0)
	v_mul_f32_e32 v2, v9, v2
	v_cndmask_b32_e64 v2, v2, -v2, s[0:1]
	v_fmac_f32_e32 v3, v232, v4
	v_fmac_f32_e32 v2, v233, v5
	v_cndmask_b32_e64 v248, v232, v3, s[2:3]
	v_cndmask_b32_e64 v249, v233, v2, s[2:3]
	s_branch .LBB0_272

.LBB0_272:
	s_waitcnt vmcnt(2)
	v_add_u32_e32 v10, 0x2000, v241
	global_load_dwordx4 v[6:9], v10, s[14:15] offset:48
	global_load_dwordx4 v[14:17], v10, s[14:15] offset:32
	global_load_dwordx4 v[2:5], v10, s[14:15] offset:16
	s_nop 0
	global_load_dwordx4 v[10:13], v10, s[14:15]
	v_lshlrev_b64 v[250:251], 1, v[222:223]
	v_lshl_add_u64 v[252:253], v[216:217], 0, v[250:251]
	v_cvt_pk_bf16_f32 v218, v218, v219
	v_cvt_pk_bf16_f32 v219, v220, v221
	v_cvt_pk_bf16_f32 v220, v230, v231
	v_cvt_pk_bf16_f32 v221, v232, v233
	global_store_dwordx4 v[252:253], v[218:221], off sc1
	v_lshl_add_u64 v[230:231], v[214:215], 0, v[250:251]
	s_and_b64 vcc, exec, s[6:7]
	v_cvt_pk_bf16_f32 v218, v242, v243
	v_cvt_pk_bf16_f32 v219, v244, v245
	v_cvt_pk_bf16_f32 v220, v246, v247
	v_cvt_pk_bf16_f32 v221, v248, v249
	global_store_dwordx4 v[230:231], v[218:221], off sc1
	v_pk_mul_f32 v[230:231], v[70:71], s[26:27] op_sel_hi:[1,0]
	v_pk_mul_f32 v[232:233], v[72:73], s[26:27] op_sel_hi:[1,0]
	v_pk_mul_f32 v[218:219], v[66:67], s[26:27] op_sel_hi:[1,0]
	v_pk_mul_f32 v[220:221], v[68:69], s[26:27] op_sel_hi:[1,0]
	s_cbranch_vccnz .LBB0_274
	v_and_b32_e32 v243, 64, v239
	v_xor_b32_e32 v242, 16, v239
	v_add_u32_e32 v243, 64, v243
	v_cmp_lt_i32_e32 vcc, v242, v243
	s_nop 1
	v_cndmask_b32_e32 v242, v239, v242, vcc
	v_lshlrev_b32_e32 v248, 2, v242
	ds_bpermute_b32 v242, v248, v218
	ds_bpermute_b32 v243, v248, v219
	s_waitcnt vmcnt(4) lgkmcnt(1)
	v_mul_f32_e32 v14, v14, v242
	v_cndmask_b32_e64 v14, v14, -v14, s[0:1]
	s_waitcnt vmcnt(2)
	v_fmac_f32_e32 v14, v218, v10
	ds_bpermute_b32 v10, v248, v220
	s_waitcnt lgkmcnt(1)
	v_mul_f32_e32 v15, v15, v243
	v_cndmask_b32_e64 v242, v218, v14, s[2:3]
	v_cndmask_b32_e64 v14, v15, -v15, s[0:1]
	v_fmac_f32_e32 v14, v219, v11
	ds_bpermute_b32 v11, v248, v221
	s_waitcnt lgkmcnt(1)
	v_mul_f32_e32 v10, v16, v10
	v_cndmask_b32_e64 v10, v10, -v10, s[0:1]
	v_fmac_f32_e32 v10, v220, v12
	v_cndmask_b32_e64 v244, v220, v10, s[2:3]
	s_waitcnt lgkmcnt(0)
	v_mul_f32_e32 v10, v17, v11
	ds_bpermute_b32 v11, v248, v230
	v_cndmask_b32_e64 v10, v10, -v10, s[0:1]
	v_fmac_f32_e32 v10, v221, v13
	v_cndmask_b32_e64 v245, v221, v10, s[2:3]
	ds_bpermute_b32 v10, v248, v231
	s_waitcnt lgkmcnt(1)
	v_mul_f32_e32 v6, v6, v11
	v_cndmask_b32_e64 v6, v6, -v6, s[0:1]
	v_fmac_f32_e32 v6, v230, v2
	v_cndmask_b32_e64 v246, v230, v6, s[2:3]
	s_waitcnt lgkmcnt(0)
	v_mul_f32_e32 v2, v7, v10
	v_cndmask_b32_e64 v2, v2, -v2, s[0:1]
	v_fmac_f32_e32 v2, v231, v3
	ds_bpermute_b32 v6, v248, v232
	v_cndmask_b32_e64 v247, v231, v2, s[2:3]
	ds_bpermute_b32 v2, v248, v233
	v_cndmask_b32_e64 v243, v219, v14, s[2:3]
	s_waitcnt lgkmcnt(1)
	v_mul_f32_e32 v3, v8, v6
	v_cndmask_b32_e64 v3, v3, -v3, s[0:1]
	s_waitcnt lgkmcnt(0)
	v_mul_f32_e32 v2, v9, v2
	v_cndmask_b32_e64 v2, v2, -v2, s[0:1]
	v_fmac_f32_e32 v3, v232, v4
	v_fmac_f32_e32 v2, v233, v5
	v_cndmask_b32_e64 v248, v232, v3, s[2:3]
	v_cndmask_b32_e64 v249, v233, v2, s[2:3]
	s_branch .LBB0_275

.LBB0_275:
	s_waitcnt vmcnt(2)
	v_add_u32_e32 v10, 0x2400, v241
	global_load_dwordx4 v[6:9], v10, s[14:15] offset:48
	global_load_dwordx4 v[14:17], v10, s[14:15] offset:32
	global_load_dwordx4 v[2:5], v10, s[14:15] offset:16
	s_nop 0
	global_load_dwordx4 v[10:13], v10, s[14:15]
	v_lshlrev_b64 v[250:251], 1, v[212:213]
	v_lshl_add_u64 v[252:253], v[216:217], 0, v[250:251]
	v_cvt_pk_bf16_f32 v218, v218, v219
	v_cvt_pk_bf16_f32 v219, v220, v221
	v_cvt_pk_bf16_f32 v220, v230, v231
	v_cvt_pk_bf16_f32 v221, v232, v233
	global_store_dwordx4 v[252:253], v[218:221], off sc1
	v_lshl_add_u64 v[230:231], v[214:215], 0, v[250:251]
	s_and_b64 vcc, exec, s[6:7]
	v_cvt_pk_bf16_f32 v218, v242, v243
	v_cvt_pk_bf16_f32 v219, v244, v245
	v_cvt_pk_bf16_f32 v220, v246, v247
	v_cvt_pk_bf16_f32 v221, v248, v249
	global_store_dwordx4 v[230:231], v[218:221], off sc1
	v_pk_mul_f32 v[230:231], v[78:79], s[26:27] op_sel_hi:[1,0]
	v_pk_mul_f32 v[232:233], v[80:81], s[26:27] op_sel_hi:[1,0]
	v_pk_mul_f32 v[218:219], v[74:75], s[26:27] op_sel_hi:[1,0]
	v_pk_mul_f32 v[220:221], v[76:77], s[26:27] op_sel_hi:[1,0]
	s_cbranch_vccnz .LBB0_277
	v_and_b32_e32 v243, 64, v239
	v_xor_b32_e32 v242, 16, v239
	v_add_u32_e32 v243, 64, v243
	v_cmp_lt_i32_e32 vcc, v242, v243
	s_nop 1
	v_cndmask_b32_e32 v242, v239, v242, vcc
	v_lshlrev_b32_e32 v248, 2, v242
	ds_bpermute_b32 v242, v248, v218
	ds_bpermute_b32 v243, v248, v219
	s_waitcnt vmcnt(4) lgkmcnt(1)
	v_mul_f32_e32 v14, v14, v242
	v_cndmask_b32_e64 v14, v14, -v14, s[0:1]
	s_waitcnt vmcnt(2)
	v_fmac_f32_e32 v14, v218, v10
	ds_bpermute_b32 v10, v248, v220
	s_waitcnt lgkmcnt(1)
	v_mul_f32_e32 v15, v15, v243
	v_cndmask_b32_e64 v242, v218, v14, s[2:3]
	v_cndmask_b32_e64 v14, v15, -v15, s[0:1]
	v_fmac_f32_e32 v14, v219, v11
	ds_bpermute_b32 v11, v248, v221
	s_waitcnt lgkmcnt(1)
	v_mul_f32_e32 v10, v16, v10
	v_cndmask_b32_e64 v10, v10, -v10, s[0:1]
	v_fmac_f32_e32 v10, v220, v12
	v_cndmask_b32_e64 v244, v220, v10, s[2:3]
	s_waitcnt lgkmcnt(0)
	v_mul_f32_e32 v10, v17, v11
	ds_bpermute_b32 v11, v248, v230
	v_cndmask_b32_e64 v10, v10, -v10, s[0:1]
	v_fmac_f32_e32 v10, v221, v13
	v_cndmask_b32_e64 v245, v221, v10, s[2:3]
	ds_bpermute_b32 v10, v248, v231
	s_waitcnt lgkmcnt(1)
	v_mul_f32_e32 v6, v6, v11
	v_cndmask_b32_e64 v6, v6, -v6, s[0:1]
	v_fmac_f32_e32 v6, v230, v2
	v_cndmask_b32_e64 v246, v230, v6, s[2:3]
	s_waitcnt lgkmcnt(0)
	v_mul_f32_e32 v2, v7, v10
	v_cndmask_b32_e64 v2, v2, -v2, s[0:1]
	v_fmac_f32_e32 v2, v231, v3
	ds_bpermute_b32 v6, v248, v232
	v_cndmask_b32_e64 v247, v231, v2, s[2:3]
	ds_bpermute_b32 v2, v248, v233
	v_cndmask_b32_e64 v243, v219, v14, s[2:3]
	s_waitcnt lgkmcnt(1)
	v_mul_f32_e32 v3, v8, v6
	v_cndmask_b32_e64 v3, v3, -v3, s[0:1]
	s_waitcnt lgkmcnt(0)
	v_mul_f32_e32 v2, v9, v2
	v_cndmask_b32_e64 v2, v2, -v2, s[0:1]
	v_fmac_f32_e32 v3, v232, v4
	v_fmac_f32_e32 v2, v233, v5
	v_cndmask_b32_e64 v248, v232, v3, s[2:3]
	v_cndmask_b32_e64 v249, v233, v2, s[2:3]
	s_branch .LBB0_278

.LBB0_278:
	s_waitcnt vmcnt(2)
	v_add_u32_e32 v10, 0x2800, v241
	global_load_dwordx4 v[6:9], v10, s[14:15] offset:48
	global_load_dwordx4 v[14:17], v10, s[14:15] offset:32
	global_load_dwordx4 v[2:5], v10, s[14:15] offset:16
	s_nop 0
	global_load_dwordx4 v[10:13], v10, s[14:15]
	v_lshlrev_b64 v[250:251], 1, v[210:211]
	v_lshl_add_u64 v[252:253], v[216:217], 0, v[250:251]
	v_cvt_pk_bf16_f32 v218, v218, v219
	v_cvt_pk_bf16_f32 v219, v220, v221
	v_cvt_pk_bf16_f32 v220, v230, v231
	v_cvt_pk_bf16_f32 v221, v232, v233
	global_store_dwordx4 v[252:253], v[218:221], off sc1
	v_lshl_add_u64 v[230:231], v[214:215], 0, v[250:251]
	s_and_b64 vcc, exec, s[6:7]
	v_cvt_pk_bf16_f32 v218, v242, v243
	v_cvt_pk_bf16_f32 v219, v244, v245
	v_cvt_pk_bf16_f32 v220, v246, v247
	v_cvt_pk_bf16_f32 v221, v248, v249
	global_store_dwordx4 v[230:231], v[218:221], off sc1
	v_pk_mul_f32 v[230:231], v[86:87], s[26:27] op_sel_hi:[1,0]
	v_pk_mul_f32 v[232:233], v[88:89], s[26:27] op_sel_hi:[1,0]
	v_pk_mul_f32 v[218:219], v[82:83], s[26:27] op_sel_hi:[1,0]
	v_pk_mul_f32 v[220:221], v[84:85], s[26:27] op_sel_hi:[1,0]
	s_cbranch_vccnz .LBB0_280
	v_and_b32_e32 v243, 64, v239
	v_xor_b32_e32 v242, 16, v239
	v_add_u32_e32 v243, 64, v243
	v_cmp_lt_i32_e32 vcc, v242, v243
	s_nop 1
	v_cndmask_b32_e32 v242, v239, v242, vcc
	v_lshlrev_b32_e32 v248, 2, v242
	ds_bpermute_b32 v242, v248, v218
	ds_bpermute_b32 v243, v248, v219
	s_waitcnt vmcnt(4) lgkmcnt(1)
	v_mul_f32_e32 v14, v14, v242
	v_cndmask_b32_e64 v14, v14, -v14, s[0:1]
	s_waitcnt vmcnt(2)
	v_fmac_f32_e32 v14, v218, v10
	ds_bpermute_b32 v10, v248, v220
	s_waitcnt lgkmcnt(1)
	v_mul_f32_e32 v15, v15, v243
	v_cndmask_b32_e64 v242, v218, v14, s[2:3]
	v_cndmask_b32_e64 v14, v15, -v15, s[0:1]
	v_fmac_f32_e32 v14, v219, v11
	ds_bpermute_b32 v11, v248, v221
	s_waitcnt lgkmcnt(1)
	v_mul_f32_e32 v10, v16, v10
	v_cndmask_b32_e64 v10, v10, -v10, s[0:1]
	v_fmac_f32_e32 v10, v220, v12
	v_cndmask_b32_e64 v244, v220, v10, s[2:3]
	s_waitcnt lgkmcnt(0)
	v_mul_f32_e32 v10, v17, v11
	ds_bpermute_b32 v11, v248, v230
	v_cndmask_b32_e64 v10, v10, -v10, s[0:1]
	v_fmac_f32_e32 v10, v221, v13
	v_cndmask_b32_e64 v245, v221, v10, s[2:3]
	ds_bpermute_b32 v10, v248, v231
	s_waitcnt lgkmcnt(1)
	v_mul_f32_e32 v6, v6, v11
	v_cndmask_b32_e64 v6, v6, -v6, s[0:1]
	v_fmac_f32_e32 v6, v230, v2
	v_cndmask_b32_e64 v246, v230, v6, s[2:3]
	s_waitcnt lgkmcnt(0)
	v_mul_f32_e32 v2, v7, v10
	v_cndmask_b32_e64 v2, v2, -v2, s[0:1]
	v_fmac_f32_e32 v2, v231, v3
	ds_bpermute_b32 v6, v248, v232
	v_cndmask_b32_e64 v247, v231, v2, s[2:3]
	ds_bpermute_b32 v2, v248, v233
	v_cndmask_b32_e64 v243, v219, v14, s[2:3]
	s_waitcnt lgkmcnt(1)
	v_mul_f32_e32 v3, v8, v6
	v_cndmask_b32_e64 v3, v3, -v3, s[0:1]
	s_waitcnt lgkmcnt(0)
	v_mul_f32_e32 v2, v9, v2
	v_cndmask_b32_e64 v2, v2, -v2, s[0:1]
	v_fmac_f32_e32 v3, v232, v4
	v_fmac_f32_e32 v2, v233, v5
	v_cndmask_b32_e64 v248, v232, v3, s[2:3]
	v_cndmask_b32_e64 v249, v233, v2, s[2:3]
	s_branch .LBB0_281

.LBB0_281:
	s_waitcnt vmcnt(2)
	v_add_u32_e32 v10, 0x2c00, v241
	global_load_dwordx4 v[6:9], v10, s[14:15] offset:48
	global_load_dwordx4 v[14:17], v10, s[14:15] offset:32
	global_load_dwordx4 v[2:5], v10, s[14:15] offset:16
	s_nop 0
	global_load_dwordx4 v[10:13], v10, s[14:15]
	v_lshlrev_b64 v[250:251], 1, v[208:209]
	v_lshl_add_u64 v[252:253], v[216:217], 0, v[250:251]
	v_cvt_pk_bf16_f32 v218, v218, v219
	v_cvt_pk_bf16_f32 v219, v220, v221
	v_cvt_pk_bf16_f32 v220, v230, v231
	v_cvt_pk_bf16_f32 v221, v232, v233
	global_store_dwordx4 v[252:253], v[218:221], off sc1
	v_lshl_add_u64 v[230:231], v[214:215], 0, v[250:251]
	s_and_b64 vcc, exec, s[6:7]
	v_cvt_pk_bf16_f32 v218, v242, v243
	v_cvt_pk_bf16_f32 v219, v244, v245
	v_cvt_pk_bf16_f32 v220, v246, v247
	v_cvt_pk_bf16_f32 v221, v248, v249
	global_store_dwordx4 v[230:231], v[218:221], off sc1
	v_pk_mul_f32 v[230:231], v[94:95], s[26:27] op_sel_hi:[1,0]
	v_pk_mul_f32 v[232:233], v[96:97], s[26:27] op_sel_hi:[1,0]
	v_pk_mul_f32 v[218:219], v[90:91], s[26:27] op_sel_hi:[1,0]
	v_pk_mul_f32 v[220:221], v[92:93], s[26:27] op_sel_hi:[1,0]
	s_cbranch_vccnz .LBB0_283
	v_and_b32_e32 v242, 64, v239
	v_xor_b32_e32 v241, 16, v239
	v_add_u32_e32 v242, 64, v242
	v_cmp_lt_i32_e32 vcc, v241, v242
	s_nop 1
	v_cndmask_b32_e32 v241, v239, v241, vcc
	v_lshlrev_b32_e32 v241, 2, v241
	ds_bpermute_b32 v242, v241, v218
	ds_bpermute_b32 v243, v241, v219
	s_waitcnt vmcnt(4) lgkmcnt(1)
	v_mul_f32_e32 v14, v14, v242
	v_cndmask_b32_e64 v14, v14, -v14, s[0:1]
	s_waitcnt vmcnt(2)
	v_fmac_f32_e32 v14, v218, v10
	s_waitcnt lgkmcnt(0)
	v_mul_f32_e32 v15, v15, v243
	v_cndmask_b32_e64 v10, v218, v14, s[2:3]
	ds_bpermute_b32 v14, v241, v220
	v_cndmask_b32_e64 v15, v15, -v15, s[0:1]
	v_fmac_f32_e32 v15, v219, v11
	v_cndmask_b32_e64 v11, v219, v15, s[2:3]
	ds_bpermute_b32 v15, v241, v221
	s_waitcnt lgkmcnt(1)
	v_mul_f32_e32 v14, v16, v14
	v_cndmask_b32_e64 v14, v14, -v14, s[0:1]
	v_fmac_f32_e32 v14, v220, v12
	v_cndmask_b32_e64 v12, v220, v14, s[2:3]
	s_waitcnt lgkmcnt(0)
	v_mul_f32_e32 v14, v17, v15
	ds_bpermute_b32 v15, v241, v230
	v_cndmask_b32_e64 v14, v14, -v14, s[0:1]
	v_fmac_f32_e32 v14, v221, v13
	v_cndmask_b32_e64 v13, v221, v14, s[2:3]
	ds_bpermute_b32 v14, v241, v231
	s_waitcnt lgkmcnt(1)
	v_mul_f32_e32 v6, v6, v15
	v_cndmask_b32_e64 v6, v6, -v6, s[0:1]
	v_fmac_f32_e32 v6, v230, v2
	v_cndmask_b32_e64 v2, v230, v6, s[2:3]
	s_waitcnt lgkmcnt(0)
	v_mul_f32_e32 v6, v7, v14
	v_cndmask_b32_e64 v6, v6, -v6, s[0:1]
	v_fmac_f32_e32 v6, v231, v3
	ds_bpermute_b32 v7, v241, v232
	v_cndmask_b32_e64 v3, v231, v6, s[2:3]
	ds_bpermute_b32 v6, v241, v233
	s_waitcnt lgkmcnt(1)
	v_mul_f32_e32 v7, v8, v7
	v_cndmask_b32_e64 v7, v7, -v7, s[0:1]
	s_waitcnt lgkmcnt(0)
	v_mul_f32_e32 v6, v9, v6
	v_cndmask_b32_e64 v6, v6, -v6, s[0:1]
	v_fmac_f32_e32 v7, v232, v4
	v_fmac_f32_e32 v6, v233, v5
	v_cndmask_b32_e64 v4, v232, v7, s[2:3]
	v_cndmask_b32_e64 v5, v233, v6, s[2:3]
	s_branch .LBB0_284

.LBB0_284:
	v_lshlrev_b64 v[14:15], 1, v[206:207]
	v_lshl_add_u64 v[16:17], v[216:217], 0, v[14:15]
	v_cvt_pk_bf16_f32 v6, v218, v219
	v_cvt_pk_bf16_f32 v7, v220, v221
	v_cvt_pk_bf16_f32 v8, v230, v231
	v_cvt_pk_bf16_f32 v9, v232, v233
	global_store_dwordx4 v[16:17], v[6:9], off sc1
	v_lshl_add_u64 v[14:15], v[214:215], 0, v[14:15]
	s_nop 0
	v_cvt_pk_bf16_f32 v6, v10, v11
	v_cvt_pk_bf16_f32 v7, v12, v13
	v_cvt_pk_bf16_f32 v8, v2, v3
	v_cvt_pk_bf16_f32 v9, v4, v5
	global_store_dwordx4 v[14:15], v[6:9], off sc1
	s_or_b32 s31, s29, 1
	s_cmp_lt_i32 s31, 4
	s_mov_b64 s[42:43], -1
	s_cbranch_scc1 .LBB0_258
.LBB0_285:
	s_cmp_lt_u32 s29, 10
	s_cbranch_scc1 .LBB0_297
	s_cmp_lt_u32 s29, 14
	s_cbranch_scc1 .LBB0_294
	s_cmp_lt_u32 s29, 22
	s_cbranch_scc1 .LBB0_291
	s_cmp_gt_u32 s29, 37
	s_cbranch_scc1 .LBB0_290
	v_mul_f32_e32 v8, 0xbfb8aa3b, v166
	v_exp_f32_e32 v8, v8
	v_mul_f32_e32 v9, 0xbfb8aa3b, v167
	v_exp_f32_e32 v9, v9
	v_mul_f32_e32 v4, 0xbfb8aa3b, v162
	v_add_f32_e32 v8, 1.0, v8
	s_waitcnt vmcnt(0)
	v_rcp_f32_e32 v10, v8
	v_add_f32_e32 v8, 1.0, v9
	v_mul_f32_e32 v9, 0xbfb8aa3b, v168
	v_mul_f32_e32 v5, 0xbfb8aa3b, v163
	v_mul_f32_e32 v6, 0xbfb8aa3b, v164
	v_mul_f32_e32 v7, 0xbfb8aa3b, v165
	v_exp_f32_e32 v9, v9
	v_mul_f32_e32 v11, 0xbfb8aa3b, v169
	s_sub_i32 s33, s29, 21
	v_exp_f32_e32 v4, v4
	v_exp_f32_e32 v5, v5
	v_exp_f32_e32 v6, v6
	v_exp_f32_e32 v7, v7
	v_exp_f32_e32 v11, v11
	s_lshr_b32 s8, s33, 3
	s_lshl_b64 s[42:43], s[8:9], 26
	s_add_u32 s8, s80, s42
	v_rcp_f32_e32 v12, v8
	v_add_f32_e32 v8, 1.0, v9
	s_addc_u32 s43, s81, s43
	s_lshl_b32 s33, s33, 8
	v_add_f32_e32 v4, 1.0, v4
	v_add_f32_e32 v5, 1.0, v5
	v_add_f32_e32 v6, 1.0, v6
	v_add_f32_e32 v7, 1.0, v7
	v_rcp_f32_e32 v13, v8
	v_add_f32_e32 v8, 1.0, v11
	s_and_b32 s33, s33, 0x700
	v_mov_b32_e32 v2, v235
	v_mov_b32_e32 v3, v240
	v_rcp_f32_e32 v4, v4
	v_rcp_f32_e32 v5, v5
	v_rcp_f32_e32 v6, v6
	v_rcp_f32_e32 v7, v7
	v_rcp_f32_e32 v11, v8
	s_add_u32 s42, s8, s33
	s_addc_u32 s43, s43, 0
	v_ashrrev_i32_e32 v3, 31, v2
	v_lshl_add_u64 v[2:3], v[2:3], 1, s[42:43]
	v_lshl_add_u64 v[8:9], v[2:3], 0, v[64:65]
	v_cvt_pk_bf16_f32 v4, v4, v5
	v_cvt_pk_bf16_f32 v5, v6, v7
	v_cvt_pk_bf16_f32 v6, v10, v12
	v_cvt_pk_bf16_f32 v7, v13, v11
	global_store_dwordx4 v[8:9], v[4:7], off sc1
	v_mul_f32_e32 v8, 0xbfb8aa3b, v174
	v_mul_f32_e32 v10, 0xbfb8aa3b, v170
	v_exp_f32_e32 v8, v8
	v_mul_f32_e32 v9, 0xbfb8aa3b, v175
	v_exp_f32_e32 v10, v10
	v_mul_f32_e32 v11, 0xbfb8aa3b, v171
	v_exp_f32_e32 v9, v9
	v_exp_f32_e32 v11, v11
	v_add_f32_e32 v8, 1.0, v8
	v_add_f32_e32 v4, 1.0, v10
	v_rcp_f32_e32 v10, v8
	v_add_f32_e32 v8, 1.0, v9
	v_mul_f32_e32 v9, 0xbfb8aa3b, v176
	v_add_f32_e32 v5, 1.0, v11
	v_mul_f32_e32 v6, 0xbfb8aa3b, v172
	v_mul_f32_e32 v7, 0xbfb8aa3b, v173
	v_exp_f32_e32 v9, v9
	v_mul_f32_e32 v11, 0xbfb8aa3b, v177
	v_exp_f32_e32 v6, v6
	v_exp_f32_e32 v7, v7
	v_exp_f32_e32 v11, v11
	v_rcp_f32_e32 v12, v8
	v_add_f32_e32 v8, 1.0, v9
	v_add_f32_e32 v6, 1.0, v6
	v_add_f32_e32 v7, 1.0, v7
	v_rcp_f32_e32 v13, v8
	v_add_f32_e32 v8, 1.0, v11
	v_rcp_f32_e32 v4, v4
	v_rcp_f32_e32 v5, v5
	v_rcp_f32_e32 v6, v6
	v_rcp_f32_e32 v7, v7
	v_rcp_f32_e32 v11, v8
	v_lshl_add_u64 v[8:9], v[2:3], 0, v[62:63]
	v_cvt_pk_bf16_f32 v4, v4, v5
	v_cvt_pk_bf16_f32 v5, v6, v7
	v_cvt_pk_bf16_f32 v6, v10, v12
	v_cvt_pk_bf16_f32 v7, v13, v11
	global_store_dwordx4 v[8:9], v[4:7], off sc1
	v_mul_f32_e32 v8, 0xbfb8aa3b, v182
	v_mul_f32_e32 v10, 0xbfb8aa3b, v178
	v_exp_f32_e32 v8, v8
	v_mul_f32_e32 v9, 0xbfb8aa3b, v183
	v_exp_f32_e32 v10, v10
	v_mul_f32_e32 v11, 0xbfb8aa3b, v179
	v_exp_f32_e32 v9, v9
	v_exp_f32_e32 v11, v11
	v_add_f32_e32 v8, 1.0, v8
	v_add_f32_e32 v4, 1.0, v10
	v_rcp_f32_e32 v10, v8
	v_add_f32_e32 v8, 1.0, v9
	v_mul_f32_e32 v9, 0xbfb8aa3b, v184
	v_add_f32_e32 v5, 1.0, v11
	v_mul_f32_e32 v6, 0xbfb8aa3b, v180
	v_mul_f32_e32 v7, 0xbfb8aa3b, v181
	v_exp_f32_e32 v9, v9
	v_mul_f32_e32 v11, 0xbfb8aa3b, v185
	v_exp_f32_e32 v6, v6
	v_exp_f32_e32 v7, v7
	v_exp_f32_e32 v11, v11
	v_rcp_f32_e32 v12, v8
	v_add_f32_e32 v8, 1.0, v9
	v_add_f32_e32 v6, 1.0, v6
	v_add_f32_e32 v7, 1.0, v7
	v_rcp_f32_e32 v13, v8
	v_add_f32_e32 v8, 1.0, v11
	v_rcp_f32_e32 v4, v4
	v_rcp_f32_e32 v5, v5
	v_rcp_f32_e32 v6, v6
	v_rcp_f32_e32 v7, v7
	v_rcp_f32_e32 v11, v8
	v_lshl_add_u64 v[8:9], v[2:3], 0, v[60:61]
	v_cvt_pk_bf16_f32 v4, v4, v5
	v_cvt_pk_bf16_f32 v5, v6, v7
	v_cvt_pk_bf16_f32 v6, v10, v12
	v_cvt_pk_bf16_f32 v7, v13, v11
	global_store_dwordx4 v[8:9], v[4:7], off sc1
	v_mul_f32_e32 v8, 0xbfb8aa3b, v190
	v_mul_f32_e32 v10, 0xbfb8aa3b, v186
	v_exp_f32_e32 v8, v8
	v_mul_f32_e32 v9, 0xbfb8aa3b, v191
	v_exp_f32_e32 v10, v10
	v_mul_f32_e32 v11, 0xbfb8aa3b, v187
	v_exp_f32_e32 v9, v9
	v_exp_f32_e32 v11, v11
	v_add_f32_e32 v8, 1.0, v8
	v_add_f32_e32 v4, 1.0, v10
	v_rcp_f32_e32 v10, v8
	v_add_f32_e32 v8, 1.0, v9
	v_mul_f32_e32 v9, 0xbfb8aa3b, v192
	v_add_f32_e32 v5, 1.0, v11
	v_mul_f32_e32 v6, 0xbfb8aa3b, v188
	v_mul_f32_e32 v7, 0xbfb8aa3b, v189
	v_exp_f32_e32 v9, v9
	v_mul_f32_e32 v11, 0xbfb8aa3b, v193
	v_exp_f32_e32 v6, v6
	v_exp_f32_e32 v7, v7
	v_exp_f32_e32 v11, v11
	v_rcp_f32_e32 v12, v8
	v_add_f32_e32 v8, 1.0, v9
	v_add_f32_e32 v6, 1.0, v6
	v_add_f32_e32 v7, 1.0, v7
	v_rcp_f32_e32 v13, v8
	v_add_f32_e32 v8, 1.0, v11
	v_rcp_f32_e32 v4, v4
	v_rcp_f32_e32 v5, v5
	v_rcp_f32_e32 v6, v6
	v_rcp_f32_e32 v7, v7
	v_rcp_f32_e32 v11, v8
	v_lshl_add_u64 v[8:9], v[2:3], 0, v[58:59]
	v_cvt_pk_bf16_f32 v4, v4, v5
	v_cvt_pk_bf16_f32 v5, v6, v7
	v_cvt_pk_bf16_f32 v6, v10, v12
	v_cvt_pk_bf16_f32 v7, v13, v11
	global_store_dwordx4 v[8:9], v[4:7], off sc1
	v_mul_f32_e32 v8, 0xbfb8aa3b, v102
	v_mul_f32_e32 v10, 0xbfb8aa3b, v98
	v_exp_f32_e32 v8, v8
	v_mul_f32_e32 v9, 0xbfb8aa3b, v103
	v_exp_f32_e32 v10, v10
	v_mul_f32_e32 v11, 0xbfb8aa3b, v99
	v_exp_f32_e32 v9, v9
	v_exp_f32_e32 v11, v11
	v_add_f32_e32 v8, 1.0, v8
	v_add_f32_e32 v4, 1.0, v10
	v_rcp_f32_e32 v10, v8
	v_add_f32_e32 v8, 1.0, v9
	v_mul_f32_e32 v9, 0xbfb8aa3b, v104
	v_add_f32_e32 v5, 1.0, v11
	v_mul_f32_e32 v6, 0xbfb8aa3b, v100
	v_mul_f32_e32 v7, 0xbfb8aa3b, v101
	v_exp_f32_e32 v9, v9
	v_mul_f32_e32 v11, 0xbfb8aa3b, v105
	v_exp_f32_e32 v6, v6
	v_exp_f32_e32 v7, v7
	v_exp_f32_e32 v11, v11
	v_rcp_f32_e32 v12, v8
	v_add_f32_e32 v8, 1.0, v9
	v_add_f32_e32 v6, 1.0, v6
	v_add_f32_e32 v7, 1.0, v7
	v_rcp_f32_e32 v13, v8
	v_add_f32_e32 v8, 1.0, v11
	v_rcp_f32_e32 v4, v4
	v_rcp_f32_e32 v5, v5
	v_rcp_f32_e32 v6, v6
	v_rcp_f32_e32 v7, v7
	v_rcp_f32_e32 v11, v8
	v_lshl_add_u64 v[8:9], v[2:3], 0, v[56:57]
	v_cvt_pk_bf16_f32 v4, v4, v5
	v_cvt_pk_bf16_f32 v5, v6, v7
	v_cvt_pk_bf16_f32 v6, v10, v12
	v_cvt_pk_bf16_f32 v7, v13, v11
	global_store_dwordx4 v[8:9], v[4:7], off sc1
	v_mul_f32_e32 v8, 0xbfb8aa3b, v118
	v_mul_f32_e32 v10, 0xbfb8aa3b, v110
	v_exp_f32_e32 v8, v8
	v_mul_f32_e32 v9, 0xbfb8aa3b, v119
	v_exp_f32_e32 v10, v10
	v_mul_f32_e32 v11, 0xbfb8aa3b, v111
	v_exp_f32_e32 v9, v9
	v_exp_f32_e32 v11, v11
	v_add_f32_e32 v8, 1.0, v8
	v_add_f32_e32 v4, 1.0, v10
	v_rcp_f32_e32 v10, v8
	v_add_f32_e32 v8, 1.0, v9
	v_mul_f32_e32 v9, 0xbfb8aa3b, v120
	v_add_f32_e32 v5, 1.0, v11
	v_mul_f32_e32 v6, 0xbfb8aa3b, v112
	v_mul_f32_e32 v7, 0xbfb8aa3b, v113
	v_exp_f32_e32 v9, v9
	v_mul_f32_e32 v11, 0xbfb8aa3b, v121
	v_exp_f32_e32 v6, v6
	v_exp_f32_e32 v7, v7
	v_exp_f32_e32 v11, v11
	v_rcp_f32_e32 v12, v8
	v_add_f32_e32 v8, 1.0, v9
	v_add_f32_e32 v6, 1.0, v6
	v_add_f32_e32 v7, 1.0, v7
	v_rcp_f32_e32 v13, v8
	v_add_f32_e32 v8, 1.0, v11
	v_rcp_f32_e32 v4, v4
	v_rcp_f32_e32 v5, v5
	v_rcp_f32_e32 v6, v6
	v_rcp_f32_e32 v7, v7
	v_rcp_f32_e32 v11, v8
	v_lshl_add_u64 v[8:9], v[2:3], 0, v[54:55]
	v_cvt_pk_bf16_f32 v4, v4, v5
	v_cvt_pk_bf16_f32 v5, v6, v7
	v_cvt_pk_bf16_f32 v6, v10, v12
	v_cvt_pk_bf16_f32 v7, v13, v11
	global_store_dwordx4 v[8:9], v[4:7], off sc1
	v_mul_f32_e32 v8, 0xbfb8aa3b, v142
	v_mul_f32_e32 v10, 0xbfb8aa3b, v130
	v_exp_f32_e32 v8, v8
	v_mul_f32_e32 v9, 0xbfb8aa3b, v143
	v_exp_f32_e32 v10, v10
	v_mul_f32_e32 v11, 0xbfb8aa3b, v131
	v_exp_f32_e32 v9, v9
	v_exp_f32_e32 v11, v11
	v_add_f32_e32 v8, 1.0, v8
	v_add_f32_e32 v4, 1.0, v10
	v_rcp_f32_e32 v10, v8
	v_add_f32_e32 v8, 1.0, v9
	v_mul_f32_e32 v9, 0xbfb8aa3b, v144
	v_add_f32_e32 v5, 1.0, v11
	v_mul_f32_e32 v6, 0xbfb8aa3b, v132
	v_mul_f32_e32 v7, 0xbfb8aa3b, v133
	v_exp_f32_e32 v9, v9
	v_mul_f32_e32 v11, 0xbfb8aa3b, v145
	v_exp_f32_e32 v6, v6
	v_exp_f32_e32 v7, v7
	v_exp_f32_e32 v11, v11
	v_rcp_f32_e32 v12, v8
	v_add_f32_e32 v8, 1.0, v9
	v_add_f32_e32 v6, 1.0, v6
	v_add_f32_e32 v7, 1.0, v7
	v_rcp_f32_e32 v13, v8
	v_add_f32_e32 v8, 1.0, v11
	v_rcp_f32_e32 v4, v4
	v_rcp_f32_e32 v5, v5
	v_rcp_f32_e32 v6, v6
	v_rcp_f32_e32 v7, v7
	v_rcp_f32_e32 v11, v8
	v_lshl_add_u64 v[8:9], v[2:3], 0, v[52:53]
	v_cvt_pk_bf16_f32 v4, v4, v5
	v_cvt_pk_bf16_f32 v5, v6, v7
	v_cvt_pk_bf16_f32 v6, v10, v12
	v_cvt_pk_bf16_f32 v7, v13, v11
	global_store_dwordx4 v[8:9], v[4:7], off sc1
	v_mul_f32_e32 v10, 0xbfb8aa3b, v150
	v_exp_f32_e32 v10, v10
	v_mul_f32_e32 v6, 0xbfb8aa3b, v152
	v_exp_f32_e32 v6, v6
	v_mul_f32_e32 v7, 0xbfb8aa3b, v153
	v_exp_f32_e32 v7, v7
	v_mul_f32_e32 v11, 0xbfb8aa3b, v151
	v_add_f32_e32 v6, 1.0, v6
	v_rcp_f32_e32 v8, v6
	v_add_f32_e32 v6, 1.0, v7
	v_mul_f32_e32 v7, 0xbfb8aa3b, v154
	v_exp_f32_e32 v7, v7
	v_mul_f32_e32 v9, 0xbfb8aa3b, v155
	v_exp_f32_e32 v11, v11
	v_exp_f32_e32 v9, v9
	v_add_f32_e32 v4, 1.0, v10
	v_rcp_f32_e32 v10, v6
	v_add_f32_e32 v6, 1.0, v7
	v_mul_f32_e32 v7, 0xbfb8aa3b, v156
	v_add_f32_e32 v5, 1.0, v11
	v_rcp_f32_e32 v11, v6
	v_add_f32_e32 v6, 1.0, v9
	v_exp_f32_e32 v7, v7
	v_mul_f32_e32 v9, 0xbfb8aa3b, v157
	v_exp_f32_e32 v9, v9
	v_rcp_f32_e32 v12, v6
	v_add_f32_e32 v6, 1.0, v7
	v_rcp_f32_e32 v13, v6
	v_add_f32_e32 v6, 1.0, v9
	v_rcp_f32_e32 v4, v4
	v_rcp_f32_e32 v5, v5
	v_rcp_f32_e32 v9, v6
	v_lshl_add_u64 v[6:7], v[2:3], 0, v[50:51]
	v_cvt_pk_bf16_f32 v3, v8, v10
	v_cvt_pk_bf16_f32 v2, v4, v5
	v_cvt_pk_bf16_f32 v4, v11, v12
	v_cvt_pk_bf16_f32 v5, v13, v9
	global_store_dwordx4 v[6:7], v[2:5], off sc1

.LBB0_291:
	s_andn2_b64 vcc, exec, s[42:43]
	s_cbranch_vccnz .LBB0_293
	s_add_i32 s33, s29, -9
	s_lshr_b32 s8, s33, 2
	s_lshl_b64 s[42:43], s[8:9], 25
	s_add_u32 s8, s76, s42
	s_addc_u32 s43, s77, s43
	s_lshl_b32 s33, s33, 8
	s_and_b32 s33, s33, 0x300
	v_mov_b32_e32 v2, v235
	v_mov_b32_e32 v3, v240
	s_add_u32 s42, s8, s33
	s_addc_u32 s43, s43, 0
	v_ashrrev_i32_e32 v3, 31, v2
	v_lshl_add_u64 v[6:7], v[2:3], 1, s[42:43]
	v_lshl_add_u64 v[8:9], v[6:7], 0, v[48:49]
	v_cvt_pk_bf16_f32 v2, v162, v163
	v_cvt_pk_bf16_f32 v3, v164, v165
	v_cvt_pk_bf16_f32 v4, v166, v167
	v_cvt_pk_bf16_f32 v5, v168, v169
	global_store_dwordx4 v[8:9], v[2:5], off sc1
	v_lshl_add_u64 v[8:9], v[6:7], 0, v[46:47]
	s_nop 0
	v_cvt_pk_bf16_f32 v2, v170, v171
	v_cvt_pk_bf16_f32 v3, v172, v173
	v_cvt_pk_bf16_f32 v4, v174, v175
	v_cvt_pk_bf16_f32 v5, v176, v177
	global_store_dwordx4 v[8:9], v[2:5], off sc1
	v_lshl_add_u64 v[8:9], v[6:7], 0, v[44:45]
	s_nop 0
	v_cvt_pk_bf16_f32 v2, v178, v179
	v_cvt_pk_bf16_f32 v3, v180, v181
	v_cvt_pk_bf16_f32 v4, v182, v183
	v_cvt_pk_bf16_f32 v5, v184, v185
	global_store_dwordx4 v[8:9], v[2:5], off sc1
	v_lshl_add_u64 v[8:9], v[6:7], 0, v[42:43]
	s_nop 0
	v_cvt_pk_bf16_f32 v2, v186, v187
	v_cvt_pk_bf16_f32 v3, v188, v189
	v_cvt_pk_bf16_f32 v4, v190, v191
	v_cvt_pk_bf16_f32 v5, v192, v193
	global_store_dwordx4 v[8:9], v[2:5], off sc1
	v_lshl_add_u64 v[8:9], v[6:7], 0, v[40:41]
	s_nop 0
	v_cvt_pk_bf16_f32 v2, v98, v99
	v_cvt_pk_bf16_f32 v3, v100, v101
	v_cvt_pk_bf16_f32 v4, v102, v103
	v_cvt_pk_bf16_f32 v5, v104, v105
	global_store_dwordx4 v[8:9], v[2:5], off sc1
	v_lshl_add_u64 v[8:9], v[6:7], 0, v[38:39]
	s_nop 0
	v_cvt_pk_bf16_f32 v2, v110, v111
	v_cvt_pk_bf16_f32 v3, v112, v113
	v_cvt_pk_bf16_f32 v4, v118, v119
	v_cvt_pk_bf16_f32 v5, v120, v121
	global_store_dwordx4 v[8:9], v[2:5], off sc1
	v_lshl_add_u64 v[8:9], v[6:7], 0, v[36:37]
	v_lshl_add_u64 v[6:7], v[6:7], 0, v[34:35]
	v_cvt_pk_bf16_f32 v2, v130, v131
	v_cvt_pk_bf16_f32 v3, v132, v133
	v_cvt_pk_bf16_f32 v4, v142, v143
	v_cvt_pk_bf16_f32 v5, v144, v145
	global_store_dwordx4 v[8:9], v[2:5], off sc1
	s_nop 1
	v_cvt_pk_bf16_f32 v2, v150, v151
	v_cvt_pk_bf16_f32 v3, v152, v153
	v_cvt_pk_bf16_f32 v4, v154, v155
	v_cvt_pk_bf16_f32 v5, v156, v157
	global_store_dwordx4 v[6:7], v[2:5], off sc1

.LBB0_294:
	s_andn2_b64 vcc, exec, s[42:43]
	s_cbranch_vccnz .LBB0_296
	s_lshl_b32 s8, s31, 8
	v_mov_b32_e32 v2, v235
	v_mov_b32_e32 v3, v240
	s_add_u32 s42, s76, s8
	s_addc_u32 s43, s77, 0
	v_ashrrev_i32_e32 v3, 31, v2
	v_lshl_add_u64 v[6:7], v[2:3], 1, s[42:43]
	v_pk_mul_f32 v[2:3], v[162:163], s[26:27] op_sel_hi:[1,0]
	v_pk_mul_f32 v[4:5], v[164:165], s[26:27] op_sel_hi:[1,0]
	v_pk_mul_f32 v[8:9], v[166:167], s[26:27] op_sel_hi:[1,0]
	s_waitcnt vmcnt(0)
	v_pk_mul_f32 v[10:11], v[168:169], s[26:27] op_sel_hi:[1,0]
	v_lshl_add_u64 v[12:13], v[6:7], 0, v[48:49]
	v_cvt_pk_bf16_f32 v2, v2, v3
	v_cvt_pk_bf16_f32 v3, v4, v5
	v_cvt_pk_bf16_f32 v4, v8, v9
	v_cvt_pk_bf16_f32 v5, v10, v11
	global_store_dwordx4 v[12:13], v[2:5], off offset:-2560 sc1
	v_pk_mul_f32 v[8:9], v[174:175], s[26:27] op_sel_hi:[1,0]
	v_pk_mul_f32 v[10:11], v[176:177], s[26:27] op_sel_hi:[1,0]
	v_pk_mul_f32 v[2:3], v[170:171], s[26:27] op_sel_hi:[1,0]
	v_pk_mul_f32 v[4:5], v[172:173], s[26:27] op_sel_hi:[1,0]
	v_lshl_add_u64 v[12:13], v[6:7], 0, v[46:47]
	v_cvt_pk_bf16_f32 v2, v2, v3
	v_cvt_pk_bf16_f32 v3, v4, v5
	v_cvt_pk_bf16_f32 v4, v8, v9
	v_cvt_pk_bf16_f32 v5, v10, v11
	global_store_dwordx4 v[12:13], v[2:5], off offset:-2560 sc1
	v_pk_mul_f32 v[8:9], v[182:183], s[26:27] op_sel_hi:[1,0]
	v_pk_mul_f32 v[10:11], v[184:185], s[26:27] op_sel_hi:[1,0]
	v_pk_mul_f32 v[2:3], v[178:179], s[26:27] op_sel_hi:[1,0]
	v_pk_mul_f32 v[4:5], v[180:181], s[26:27] op_sel_hi:[1,0]
	v_lshl_add_u64 v[12:13], v[6:7], 0, v[44:45]
	v_cvt_pk_bf16_f32 v2, v2, v3
	v_cvt_pk_bf16_f32 v3, v4, v5
	v_cvt_pk_bf16_f32 v4, v8, v9
	v_cvt_pk_bf16_f32 v5, v10, v11
	global_store_dwordx4 v[12:13], v[2:5], off offset:-2560 sc1
	v_pk_mul_f32 v[8:9], v[190:191], s[26:27] op_sel_hi:[1,0]
	v_pk_mul_f32 v[10:11], v[192:193], s[26:27] op_sel_hi:[1,0]
	v_pk_mul_f32 v[2:3], v[186:187], s[26:27] op_sel_hi:[1,0]
	v_pk_mul_f32 v[4:5], v[188:189], s[26:27] op_sel_hi:[1,0]
	v_lshl_add_u64 v[12:13], v[6:7], 0, v[42:43]
	v_cvt_pk_bf16_f32 v2, v2, v3
	v_cvt_pk_bf16_f32 v3, v4, v5
	v_cvt_pk_bf16_f32 v4, v8, v9
	v_cvt_pk_bf16_f32 v5, v10, v11
	global_store_dwordx4 v[12:13], v[2:5], off offset:-2560 sc1
	v_pk_mul_f32 v[8:9], v[102:103], s[26:27] op_sel_hi:[1,0]
	v_pk_mul_f32 v[10:11], v[104:105], s[26:27] op_sel_hi:[1,0]
	v_pk_mul_f32 v[2:3], v[98:99], s[26:27] op_sel_hi:[1,0]
	v_pk_mul_f32 v[4:5], v[100:101], s[26:27] op_sel_hi:[1,0]
	v_lshl_add_u64 v[12:13], v[6:7], 0, v[40:41]
	v_cvt_pk_bf16_f32 v2, v2, v3
	v_cvt_pk_bf16_f32 v3, v4, v5
	v_cvt_pk_bf16_f32 v4, v8, v9
	v_cvt_pk_bf16_f32 v5, v10, v11
	global_store_dwordx4 v[12:13], v[2:5], off offset:-2560 sc1
	v_pk_mul_f32 v[8:9], v[118:119], s[26:27] op_sel_hi:[1,0]
	v_pk_mul_f32 v[10:11], v[120:121], s[26:27] op_sel_hi:[1,0]
	v_pk_mul_f32 v[2:3], v[110:111], s[26:27] op_sel_hi:[1,0]
	v_pk_mul_f32 v[4:5], v[112:113], s[26:27] op_sel_hi:[1,0]
	v_lshl_add_u64 v[12:13], v[6:7], 0, v[38:39]
	v_cvt_pk_bf16_f32 v2, v2, v3
	v_cvt_pk_bf16_f32 v3, v4, v5
	v_cvt_pk_bf16_f32 v4, v8, v9
	v_cvt_pk_bf16_f32 v5, v10, v11
	global_store_dwordx4 v[12:13], v[2:5], off offset:-2560 sc1
	v_pk_mul_f32 v[8:9], v[142:143], s[26:27] op_sel_hi:[1,0]
	v_pk_mul_f32 v[10:11], v[144:145], s[26:27] op_sel_hi:[1,0]
	v_pk_mul_f32 v[2:3], v[130:131], s[26:27] op_sel_hi:[1,0]
	v_pk_mul_f32 v[4:5], v[132:133], s[26:27] op_sel_hi:[1,0]
	v_lshl_add_u64 v[12:13], v[6:7], 0, v[36:37]
	v_cvt_pk_bf16_f32 v2, v2, v3
	v_cvt_pk_bf16_f32 v3, v4, v5
	v_cvt_pk_bf16_f32 v4, v8, v9
	v_cvt_pk_bf16_f32 v5, v10, v11
	global_store_dwordx4 v[12:13], v[2:5], off offset:-2560 sc1
	v_pk_mul_f32 v[8:9], v[154:155], s[26:27] op_sel_hi:[1,0]
	v_pk_mul_f32 v[10:11], v[156:157], s[26:27] op_sel_hi:[1,0]
	v_pk_mul_f32 v[2:3], v[150:151], s[26:27] op_sel_hi:[1,0]
	v_pk_mul_f32 v[4:5], v[152:153], s[26:27] op_sel_hi:[1,0]
	v_lshl_add_u64 v[6:7], v[6:7], 0, v[34:35]
	v_cvt_pk_bf16_f32 v2, v2, v3
	v_cvt_pk_bf16_f32 v3, v4, v5
	v_cvt_pk_bf16_f32 v4, v8, v9
	v_cvt_pk_bf16_f32 v5, v10, v11
	global_store_dwordx4 v[6:7], v[2:5], off offset:-2560 sc1

.LBB0_297:
	s_andn2_b64 vcc, exec, s[42:43]
	s_cbranch_vccnz .LBB0_299
	s_add_i32 s8, s29, -3
	s_lshl_b64 s[42:43], s[8:9], 23
	v_mov_b32_e32 v2, v235
	v_mov_b32_e32 v3, v240
	s_add_u32 s42, s74, s42
	s_addc_u32 s43, s75, s43
	v_ashrrev_i32_e32 v3, 31, v2
	v_lshl_add_u64 v[6:7], v[2:3], 1, s[42:43]
	v_lshl_add_u64 v[8:9], v[6:7], 0, v[32:33]
	v_cvt_pk_bf16_f32 v2, v162, v163
	v_cvt_pk_bf16_f32 v3, v164, v165
	v_cvt_pk_bf16_f32 v4, v166, v167
	v_cvt_pk_bf16_f32 v5, v168, v169
	global_store_dwordx4 v[8:9], v[2:5], off sc1
	v_lshl_add_u64 v[8:9], v[6:7], 0, v[30:31]
	s_nop 0
	v_cvt_pk_bf16_f32 v2, v170, v171
	v_cvt_pk_bf16_f32 v3, v172, v173
	v_cvt_pk_bf16_f32 v4, v174, v175
	v_cvt_pk_bf16_f32 v5, v176, v177
	global_store_dwordx4 v[8:9], v[2:5], off sc1
	v_lshl_add_u64 v[8:9], v[6:7], 0, v[28:29]
	s_nop 0
	v_cvt_pk_bf16_f32 v2, v178, v179
	v_cvt_pk_bf16_f32 v3, v180, v181
	v_cvt_pk_bf16_f32 v4, v182, v183
	v_cvt_pk_bf16_f32 v5, v184, v185
	global_store_dwordx4 v[8:9], v[2:5], off sc1
	v_lshl_add_u64 v[8:9], v[6:7], 0, v[26:27]
	s_nop 0
	v_cvt_pk_bf16_f32 v2, v186, v187
	v_cvt_pk_bf16_f32 v3, v188, v189
	v_cvt_pk_bf16_f32 v4, v190, v191
	v_cvt_pk_bf16_f32 v5, v192, v193
	global_store_dwordx4 v[8:9], v[2:5], off sc1
	v_lshl_add_u64 v[8:9], v[6:7], 0, v[24:25]
	s_nop 0
	v_cvt_pk_bf16_f32 v2, v98, v99
	v_cvt_pk_bf16_f32 v3, v100, v101
	v_cvt_pk_bf16_f32 v4, v102, v103
	v_cvt_pk_bf16_f32 v5, v104, v105
	global_store_dwordx4 v[8:9], v[2:5], off sc1
	v_lshl_add_u64 v[8:9], v[6:7], 0, v[22:23]
	s_nop 0
	v_cvt_pk_bf16_f32 v2, v110, v111
	v_cvt_pk_bf16_f32 v3, v112, v113
	v_cvt_pk_bf16_f32 v4, v118, v119
	v_cvt_pk_bf16_f32 v5, v120, v121
	global_store_dwordx4 v[8:9], v[2:5], off sc1
	v_lshl_add_u64 v[8:9], v[6:7], 0, v[20:21]
	v_lshl_add_u64 v[6:7], v[6:7], 0, v[18:19]
	v_cvt_pk_bf16_f32 v2, v130, v131
	v_cvt_pk_bf16_f32 v3, v132, v133
	v_cvt_pk_bf16_f32 v4, v142, v143
	v_cvt_pk_bf16_f32 v5, v144, v145
	global_store_dwordx4 v[8:9], v[2:5], off sc1
	s_nop 1
	v_cvt_pk_bf16_f32 v2, v150, v151
	v_cvt_pk_bf16_f32 v3, v152, v153
	v_cvt_pk_bf16_f32 v4, v154, v155
	v_cvt_pk_bf16_f32 v5, v156, v157
	global_store_dwordx4 v[6:7], v[2:5], off sc1

.LBB0_303:
	s_waitcnt vmcnt(0)
	v_add_u32_e32 v10, 0x400, v240
	global_load_dwordx4 v[6:9], v10, s[14:15] offset:48
	global_load_dwordx4 v[14:17], v10, s[14:15] offset:32
	global_load_dwordx4 v[2:5], v10, s[14:15] offset:16
	s_nop 0
	global_load_dwordx4 v[10:13], v10, s[14:15]
	s_lshl_b32 s42, s31, 7
	s_ashr_i32 s43, s42, 31
	s_lshl_b64 s[42:43], s[42:43], 1
	s_add_u32 s44, s70, s42
	s_addc_u32 s45, s71, s43
	v_ashrrev_i32_e32 v19, 31, v18
	s_add_u32 s42, s72, s42
	v_lshlrev_b64 v[18:19], 1, v[18:19]
	s_addc_u32 s43, s73, s43
	v_lshl_add_u64 v[20:21], s[44:45], 0, v[18:19]
	v_lshlrev_b64 v[38:39], 1, v[228:229]
	v_lshl_add_u64 v[18:19], s[42:43], 0, v[18:19]
	v_lshl_add_u64 v[40:41], v[20:21], 0, v[38:39]
	v_cvt_pk_bf16_f32 v22, v22, v23
	v_cvt_pk_bf16_f32 v23, v24, v25
	v_cvt_pk_bf16_f32 v24, v26, v27
	v_cvt_pk_bf16_f32 v25, v28, v29
	global_store_dwordx4 v[40:41], v[22:25], off sc1
	v_lshl_add_u64 v[26:27], v[18:19], 0, v[38:39]
	s_and_b64 vcc, exec, s[6:7]
	v_cvt_pk_bf16_f32 v22, v30, v31
	v_cvt_pk_bf16_f32 v23, v32, v33
	v_cvt_pk_bf16_f32 v24, v34, v35
	v_cvt_pk_bf16_f32 v25, v36, v37
	global_store_dwordx4 v[26:27], v[22:25], off sc1
	v_pk_mul_f32 v[26:27], v[174:175], s[26:27] op_sel_hi:[1,0]
	v_pk_mul_f32 v[28:29], v[176:177], s[26:27] op_sel_hi:[1,0]
	v_pk_mul_f32 v[22:23], v[170:171], s[26:27] op_sel_hi:[1,0]
	v_pk_mul_f32 v[24:25], v[172:173], s[26:27] op_sel_hi:[1,0]
	s_cbranch_vccnz .LBB0_305
	v_and_b32_e32 v31, 64, v239
	v_xor_b32_e32 v30, 16, v239
	v_add_u32_e32 v31, 64, v31
	v_cmp_lt_i32_e32 vcc, v30, v31
	s_nop 1
	v_cndmask_b32_e32 v30, v239, v30, vcc
	v_lshlrev_b32_e32 v36, 2, v30
	ds_bpermute_b32 v30, v36, v22
	ds_bpermute_b32 v31, v36, v23
	s_waitcnt vmcnt(4) lgkmcnt(1)
	v_mul_f32_e32 v14, v14, v30
	v_cndmask_b32_e64 v14, v14, -v14, s[0:1]
	s_waitcnt vmcnt(2)
	v_fmac_f32_e32 v14, v22, v10
	ds_bpermute_b32 v10, v36, v24
	s_waitcnt lgkmcnt(1)
	v_mul_f32_e32 v15, v15, v31
	v_cndmask_b32_e64 v30, v22, v14, s[2:3]
	v_cndmask_b32_e64 v14, v15, -v15, s[0:1]
	v_fmac_f32_e32 v14, v23, v11
	ds_bpermute_b32 v11, v36, v25
	s_waitcnt lgkmcnt(1)
	v_mul_f32_e32 v10, v16, v10
	v_cndmask_b32_e64 v10, v10, -v10, s[0:1]
	v_fmac_f32_e32 v10, v24, v12
	v_cndmask_b32_e64 v32, v24, v10, s[2:3]
	s_waitcnt lgkmcnt(0)
	v_mul_f32_e32 v10, v17, v11
	ds_bpermute_b32 v11, v36, v26
	v_cndmask_b32_e64 v10, v10, -v10, s[0:1]
	v_fmac_f32_e32 v10, v25, v13
	v_cndmask_b32_e64 v33, v25, v10, s[2:3]
	ds_bpermute_b32 v10, v36, v27
	s_waitcnt lgkmcnt(1)
	v_mul_f32_e32 v6, v6, v11
	v_cndmask_b32_e64 v6, v6, -v6, s[0:1]
	v_fmac_f32_e32 v6, v26, v2
	v_cndmask_b32_e64 v34, v26, v6, s[2:3]
	s_waitcnt lgkmcnt(0)
	v_mul_f32_e32 v2, v7, v10
	v_cndmask_b32_e64 v2, v2, -v2, s[0:1]
	v_fmac_f32_e32 v2, v27, v3
	ds_bpermute_b32 v6, v36, v28
	v_cndmask_b32_e64 v35, v27, v2, s[2:3]
	ds_bpermute_b32 v2, v36, v29
	v_cndmask_b32_e64 v31, v23, v14, s[2:3]
	s_waitcnt lgkmcnt(1)
	v_mul_f32_e32 v3, v8, v6
	v_cndmask_b32_e64 v3, v3, -v3, s[0:1]
	s_waitcnt lgkmcnt(0)
	v_mul_f32_e32 v2, v9, v2
	v_cndmask_b32_e64 v2, v2, -v2, s[0:1]
	v_fmac_f32_e32 v3, v28, v4
	v_fmac_f32_e32 v2, v29, v5
	v_cndmask_b32_e64 v36, v28, v3, s[2:3]
	v_cndmask_b32_e64 v37, v29, v2, s[2:3]
	s_branch .LBB0_306

.LBB0_306:
	s_waitcnt vmcnt(2)
	v_add_u32_e32 v10, 0x800, v240
	global_load_dwordx4 v[6:9], v10, s[14:15] offset:48
	global_load_dwordx4 v[14:17], v10, s[14:15] offset:32
	global_load_dwordx4 v[2:5], v10, s[14:15] offset:16
	s_nop 0
	global_load_dwordx4 v[10:13], v10, s[14:15]
	v_lshlrev_b64 v[38:39], 1, v[226:227]
	v_lshl_add_u64 v[40:41], v[20:21], 0, v[38:39]
	v_cvt_pk_bf16_f32 v22, v22, v23
	v_cvt_pk_bf16_f32 v23, v24, v25
	v_cvt_pk_bf16_f32 v24, v26, v27
	v_cvt_pk_bf16_f32 v25, v28, v29
	global_store_dwordx4 v[40:41], v[22:25], off sc1
	v_lshl_add_u64 v[26:27], v[18:19], 0, v[38:39]
	s_and_b64 vcc, exec, s[6:7]
	v_cvt_pk_bf16_f32 v22, v30, v31
	v_cvt_pk_bf16_f32 v23, v32, v33
	v_cvt_pk_bf16_f32 v24, v34, v35
	v_cvt_pk_bf16_f32 v25, v36, v37
	global_store_dwordx4 v[26:27], v[22:25], off sc1
	v_pk_mul_f32 v[26:27], v[182:183], s[26:27] op_sel_hi:[1,0]
	v_pk_mul_f32 v[28:29], v[184:185], s[26:27] op_sel_hi:[1,0]
	v_pk_mul_f32 v[22:23], v[178:179], s[26:27] op_sel_hi:[1,0]
	v_pk_mul_f32 v[24:25], v[180:181], s[26:27] op_sel_hi:[1,0]
	s_cbranch_vccnz .LBB0_308
	v_and_b32_e32 v31, 64, v239
	v_xor_b32_e32 v30, 16, v239
	v_add_u32_e32 v31, 64, v31
	v_cmp_lt_i32_e32 vcc, v30, v31
	s_nop 1
	v_cndmask_b32_e32 v30, v239, v30, vcc
	v_lshlrev_b32_e32 v36, 2, v30
	ds_bpermute_b32 v30, v36, v22
	ds_bpermute_b32 v31, v36, v23
	s_waitcnt vmcnt(4) lgkmcnt(1)
	v_mul_f32_e32 v14, v14, v30
	v_cndmask_b32_e64 v14, v14, -v14, s[0:1]
	s_waitcnt vmcnt(2)
	v_fmac_f32_e32 v14, v22, v10
	ds_bpermute_b32 v10, v36, v24
	s_waitcnt lgkmcnt(1)
	v_mul_f32_e32 v15, v15, v31
	v_cndmask_b32_e64 v30, v22, v14, s[2:3]
	v_cndmask_b32_e64 v14, v15, -v15, s[0:1]
	v_fmac_f32_e32 v14, v23, v11
	ds_bpermute_b32 v11, v36, v25
	s_waitcnt lgkmcnt(1)
	v_mul_f32_e32 v10, v16, v10
	v_cndmask_b32_e64 v10, v10, -v10, s[0:1]
	v_fmac_f32_e32 v10, v24, v12
	v_cndmask_b32_e64 v32, v24, v10, s[2:3]
	s_waitcnt lgkmcnt(0)
	v_mul_f32_e32 v10, v17, v11
	ds_bpermute_b32 v11, v36, v26
	v_cndmask_b32_e64 v10, v10, -v10, s[0:1]
	v_fmac_f32_e32 v10, v25, v13
	v_cndmask_b32_e64 v33, v25, v10, s[2:3]
	ds_bpermute_b32 v10, v36, v27
	s_waitcnt lgkmcnt(1)
	v_mul_f32_e32 v6, v6, v11
	v_cndmask_b32_e64 v6, v6, -v6, s[0:1]
	v_fmac_f32_e32 v6, v26, v2
	v_cndmask_b32_e64 v34, v26, v6, s[2:3]
	s_waitcnt lgkmcnt(0)
	v_mul_f32_e32 v2, v7, v10
	v_cndmask_b32_e64 v2, v2, -v2, s[0:1]
	v_fmac_f32_e32 v2, v27, v3
	ds_bpermute_b32 v6, v36, v28
	v_cndmask_b32_e64 v35, v27, v2, s[2:3]
	ds_bpermute_b32 v2, v36, v29
	v_cndmask_b32_e64 v31, v23, v14, s[2:3]
	s_waitcnt lgkmcnt(1)
	v_mul_f32_e32 v3, v8, v6
	v_cndmask_b32_e64 v3, v3, -v3, s[0:1]
	s_waitcnt lgkmcnt(0)
	v_mul_f32_e32 v2, v9, v2
	v_cndmask_b32_e64 v2, v2, -v2, s[0:1]
	v_fmac_f32_e32 v3, v28, v4
	v_fmac_f32_e32 v2, v29, v5
	v_cndmask_b32_e64 v36, v28, v3, s[2:3]
	v_cndmask_b32_e64 v37, v29, v2, s[2:3]
	s_branch .LBB0_309

.LBB0_309:
	s_waitcnt vmcnt(2)
	v_add_u32_e32 v10, 0xc00, v240
	global_load_dwordx4 v[6:9], v10, s[14:15] offset:48
	global_load_dwordx4 v[14:17], v10, s[14:15] offset:32
	global_load_dwordx4 v[2:5], v10, s[14:15] offset:16
	s_nop 0
	global_load_dwordx4 v[10:13], v10, s[14:15]
	v_lshlrev_b64 v[38:39], 1, v[224:225]
	v_lshl_add_u64 v[40:41], v[20:21], 0, v[38:39]
	v_cvt_pk_bf16_f32 v22, v22, v23
	v_cvt_pk_bf16_f32 v23, v24, v25
	v_cvt_pk_bf16_f32 v24, v26, v27
	v_cvt_pk_bf16_f32 v25, v28, v29
	global_store_dwordx4 v[40:41], v[22:25], off sc1
	v_lshl_add_u64 v[26:27], v[18:19], 0, v[38:39]
	s_and_b64 vcc, exec, s[6:7]
	v_cvt_pk_bf16_f32 v22, v30, v31
	v_cvt_pk_bf16_f32 v23, v32, v33
	v_cvt_pk_bf16_f32 v24, v34, v35
	v_cvt_pk_bf16_f32 v25, v36, v37
	global_store_dwordx4 v[26:27], v[22:25], off sc1
	v_pk_mul_f32 v[26:27], v[190:191], s[26:27] op_sel_hi:[1,0]
	v_pk_mul_f32 v[28:29], v[192:193], s[26:27] op_sel_hi:[1,0]
	v_pk_mul_f32 v[22:23], v[186:187], s[26:27] op_sel_hi:[1,0]
	v_pk_mul_f32 v[24:25], v[188:189], s[26:27] op_sel_hi:[1,0]
	s_cbranch_vccnz .LBB0_311
	v_and_b32_e32 v31, 64, v239
	v_xor_b32_e32 v30, 16, v239
	v_add_u32_e32 v31, 64, v31
	v_cmp_lt_i32_e32 vcc, v30, v31
	s_nop 1
	v_cndmask_b32_e32 v30, v239, v30, vcc
	v_lshlrev_b32_e32 v36, 2, v30
	ds_bpermute_b32 v30, v36, v22
	ds_bpermute_b32 v31, v36, v23
	s_waitcnt vmcnt(4) lgkmcnt(1)
	v_mul_f32_e32 v14, v14, v30
	v_cndmask_b32_e64 v14, v14, -v14, s[0:1]
	s_waitcnt vmcnt(2)
	v_fmac_f32_e32 v14, v22, v10
	ds_bpermute_b32 v10, v36, v24
	s_waitcnt lgkmcnt(1)
	v_mul_f32_e32 v15, v15, v31
	v_cndmask_b32_e64 v30, v22, v14, s[2:3]
	v_cndmask_b32_e64 v14, v15, -v15, s[0:1]
	v_fmac_f32_e32 v14, v23, v11
	ds_bpermute_b32 v11, v36, v25
	s_waitcnt lgkmcnt(1)
	v_mul_f32_e32 v10, v16, v10
	v_cndmask_b32_e64 v10, v10, -v10, s[0:1]
	v_fmac_f32_e32 v10, v24, v12
	v_cndmask_b32_e64 v32, v24, v10, s[2:3]
	s_waitcnt lgkmcnt(0)
	v_mul_f32_e32 v10, v17, v11
	ds_bpermute_b32 v11, v36, v26
	v_cndmask_b32_e64 v10, v10, -v10, s[0:1]
	v_fmac_f32_e32 v10, v25, v13
	v_cndmask_b32_e64 v33, v25, v10, s[2:3]
	ds_bpermute_b32 v10, v36, v27
	s_waitcnt lgkmcnt(1)
	v_mul_f32_e32 v6, v6, v11
	v_cndmask_b32_e64 v6, v6, -v6, s[0:1]
	v_fmac_f32_e32 v6, v26, v2
	v_cndmask_b32_e64 v34, v26, v6, s[2:3]
	s_waitcnt lgkmcnt(0)
	v_mul_f32_e32 v2, v7, v10
	v_cndmask_b32_e64 v2, v2, -v2, s[0:1]
	v_fmac_f32_e32 v2, v27, v3
	ds_bpermute_b32 v6, v36, v28
	v_cndmask_b32_e64 v35, v27, v2, s[2:3]
	ds_bpermute_b32 v2, v36, v29
	v_cndmask_b32_e64 v31, v23, v14, s[2:3]
	s_waitcnt lgkmcnt(1)
	v_mul_f32_e32 v3, v8, v6
	v_cndmask_b32_e64 v3, v3, -v3, s[0:1]
	s_waitcnt lgkmcnt(0)
	v_mul_f32_e32 v2, v9, v2
	v_cndmask_b32_e64 v2, v2, -v2, s[0:1]
	v_fmac_f32_e32 v3, v28, v4
	v_fmac_f32_e32 v2, v29, v5
	v_cndmask_b32_e64 v36, v28, v3, s[2:3]
	v_cndmask_b32_e64 v37, v29, v2, s[2:3]
	s_branch .LBB0_312

.LBB0_312:
	s_waitcnt vmcnt(2)
	v_add_u32_e32 v10, 0x2000, v240
	global_load_dwordx4 v[6:9], v10, s[14:15] offset:48
	global_load_dwordx4 v[14:17], v10, s[14:15] offset:32
	global_load_dwordx4 v[2:5], v10, s[14:15] offset:16
	s_nop 0
	global_load_dwordx4 v[10:13], v10, s[14:15]
	v_lshlrev_b64 v[38:39], 1, v[222:223]
	v_lshl_add_u64 v[40:41], v[20:21], 0, v[38:39]
	v_cvt_pk_bf16_f32 v22, v22, v23
	v_cvt_pk_bf16_f32 v23, v24, v25
	v_cvt_pk_bf16_f32 v24, v26, v27
	v_cvt_pk_bf16_f32 v25, v28, v29
	global_store_dwordx4 v[40:41], v[22:25], off sc1
	v_lshl_add_u64 v[26:27], v[18:19], 0, v[38:39]
	s_and_b64 vcc, exec, s[6:7]
	v_cvt_pk_bf16_f32 v22, v30, v31
	v_cvt_pk_bf16_f32 v23, v32, v33
	v_cvt_pk_bf16_f32 v24, v34, v35
	v_cvt_pk_bf16_f32 v25, v36, v37
	global_store_dwordx4 v[26:27], v[22:25], off sc1
	v_pk_mul_f32 v[26:27], v[102:103], s[26:27] op_sel_hi:[1,0]
	v_pk_mul_f32 v[28:29], v[104:105], s[26:27] op_sel_hi:[1,0]
	v_pk_mul_f32 v[22:23], v[98:99], s[26:27] op_sel_hi:[1,0]
	v_pk_mul_f32 v[24:25], v[100:101], s[26:27] op_sel_hi:[1,0]
	s_cbranch_vccnz .LBB0_314
	v_and_b32_e32 v31, 64, v239
	v_xor_b32_e32 v30, 16, v239
	v_add_u32_e32 v31, 64, v31
	v_cmp_lt_i32_e32 vcc, v30, v31
	s_nop 1
	v_cndmask_b32_e32 v30, v239, v30, vcc
	v_lshlrev_b32_e32 v36, 2, v30
	ds_bpermute_b32 v30, v36, v22
	ds_bpermute_b32 v31, v36, v23
	s_waitcnt vmcnt(4) lgkmcnt(1)
	v_mul_f32_e32 v14, v14, v30
	v_cndmask_b32_e64 v14, v14, -v14, s[0:1]
	s_waitcnt vmcnt(2)
	v_fmac_f32_e32 v14, v22, v10
	ds_bpermute_b32 v10, v36, v24
	s_waitcnt lgkmcnt(1)
	v_mul_f32_e32 v15, v15, v31
	v_cndmask_b32_e64 v30, v22, v14, s[2:3]
	v_cndmask_b32_e64 v14, v15, -v15, s[0:1]
	v_fmac_f32_e32 v14, v23, v11
	ds_bpermute_b32 v11, v36, v25
	s_waitcnt lgkmcnt(1)
	v_mul_f32_e32 v10, v16, v10
	v_cndmask_b32_e64 v10, v10, -v10, s[0:1]
	v_fmac_f32_e32 v10, v24, v12
	v_cndmask_b32_e64 v32, v24, v10, s[2:3]
	s_waitcnt lgkmcnt(0)
	v_mul_f32_e32 v10, v17, v11
	ds_bpermute_b32 v11, v36, v26
	v_cndmask_b32_e64 v10, v10, -v10, s[0:1]
	v_fmac_f32_e32 v10, v25, v13
	v_cndmask_b32_e64 v33, v25, v10, s[2:3]
	ds_bpermute_b32 v10, v36, v27
	s_waitcnt lgkmcnt(1)
	v_mul_f32_e32 v6, v6, v11
	v_cndmask_b32_e64 v6, v6, -v6, s[0:1]
	v_fmac_f32_e32 v6, v26, v2
	v_cndmask_b32_e64 v34, v26, v6, s[2:3]
	s_waitcnt lgkmcnt(0)
	v_mul_f32_e32 v2, v7, v10
	v_cndmask_b32_e64 v2, v2, -v2, s[0:1]
	v_fmac_f32_e32 v2, v27, v3
	ds_bpermute_b32 v6, v36, v28
	v_cndmask_b32_e64 v35, v27, v2, s[2:3]
	ds_bpermute_b32 v2, v36, v29
	v_cndmask_b32_e64 v31, v23, v14, s[2:3]
	s_waitcnt lgkmcnt(1)
	v_mul_f32_e32 v3, v8, v6
	v_cndmask_b32_e64 v3, v3, -v3, s[0:1]
	s_waitcnt lgkmcnt(0)
	v_mul_f32_e32 v2, v9, v2
	v_cndmask_b32_e64 v2, v2, -v2, s[0:1]
	v_fmac_f32_e32 v3, v28, v4
	v_fmac_f32_e32 v2, v29, v5
	v_cndmask_b32_e64 v36, v28, v3, s[2:3]
	v_cndmask_b32_e64 v37, v29, v2, s[2:3]
	s_branch .LBB0_315

.LBB0_315:
	s_waitcnt vmcnt(2)
	v_add_u32_e32 v10, 0x2400, v240
	global_load_dwordx4 v[6:9], v10, s[14:15] offset:48
	global_load_dwordx4 v[14:17], v10, s[14:15] offset:32
	global_load_dwordx4 v[2:5], v10, s[14:15] offset:16
	s_nop 0
	global_load_dwordx4 v[10:13], v10, s[14:15]
	v_lshlrev_b64 v[38:39], 1, v[212:213]
	v_lshl_add_u64 v[40:41], v[20:21], 0, v[38:39]
	v_cvt_pk_bf16_f32 v22, v22, v23
	v_cvt_pk_bf16_f32 v23, v24, v25
	v_cvt_pk_bf16_f32 v24, v26, v27
	v_cvt_pk_bf16_f32 v25, v28, v29
	global_store_dwordx4 v[40:41], v[22:25], off sc1
	v_lshl_add_u64 v[26:27], v[18:19], 0, v[38:39]
	s_and_b64 vcc, exec, s[6:7]
	v_cvt_pk_bf16_f32 v22, v30, v31
	v_cvt_pk_bf16_f32 v23, v32, v33
	v_cvt_pk_bf16_f32 v24, v34, v35
	v_cvt_pk_bf16_f32 v25, v36, v37
	global_store_dwordx4 v[26:27], v[22:25], off sc1
	v_pk_mul_f32 v[26:27], v[118:119], s[26:27] op_sel_hi:[1,0]
	v_pk_mul_f32 v[28:29], v[120:121], s[26:27] op_sel_hi:[1,0]
	v_pk_mul_f32 v[22:23], v[110:111], s[26:27] op_sel_hi:[1,0]
	v_pk_mul_f32 v[24:25], v[112:113], s[26:27] op_sel_hi:[1,0]
	s_cbranch_vccnz .LBB0_317
	v_and_b32_e32 v31, 64, v239
	v_xor_b32_e32 v30, 16, v239
	v_add_u32_e32 v31, 64, v31
	v_cmp_lt_i32_e32 vcc, v30, v31
	s_nop 1
	v_cndmask_b32_e32 v30, v239, v30, vcc
	v_lshlrev_b32_e32 v36, 2, v30
	ds_bpermute_b32 v30, v36, v22
	ds_bpermute_b32 v31, v36, v23
	s_waitcnt vmcnt(4) lgkmcnt(1)
	v_mul_f32_e32 v14, v14, v30
	v_cndmask_b32_e64 v14, v14, -v14, s[0:1]
	s_waitcnt vmcnt(2)
	v_fmac_f32_e32 v14, v22, v10
	ds_bpermute_b32 v10, v36, v24
	s_waitcnt lgkmcnt(1)
	v_mul_f32_e32 v15, v15, v31
	v_cndmask_b32_e64 v30, v22, v14, s[2:3]
	v_cndmask_b32_e64 v14, v15, -v15, s[0:1]
	v_fmac_f32_e32 v14, v23, v11
	ds_bpermute_b32 v11, v36, v25
	s_waitcnt lgkmcnt(1)
	v_mul_f32_e32 v10, v16, v10
	v_cndmask_b32_e64 v10, v10, -v10, s[0:1]
	v_fmac_f32_e32 v10, v24, v12
	v_cndmask_b32_e64 v32, v24, v10, s[2:3]
	s_waitcnt lgkmcnt(0)
	v_mul_f32_e32 v10, v17, v11
	ds_bpermute_b32 v11, v36, v26
	v_cndmask_b32_e64 v10, v10, -v10, s[0:1]
	v_fmac_f32_e32 v10, v25, v13
	v_cndmask_b32_e64 v33, v25, v10, s[2:3]
	ds_bpermute_b32 v10, v36, v27
	s_waitcnt lgkmcnt(1)
	v_mul_f32_e32 v6, v6, v11
	v_cndmask_b32_e64 v6, v6, -v6, s[0:1]
	v_fmac_f32_e32 v6, v26, v2
	v_cndmask_b32_e64 v34, v26, v6, s[2:3]
	s_waitcnt lgkmcnt(0)
	v_mul_f32_e32 v2, v7, v10
	v_cndmask_b32_e64 v2, v2, -v2, s[0:1]
	v_fmac_f32_e32 v2, v27, v3
	ds_bpermute_b32 v6, v36, v28
	v_cndmask_b32_e64 v35, v27, v2, s[2:3]
	ds_bpermute_b32 v2, v36, v29
	v_cndmask_b32_e64 v31, v23, v14, s[2:3]
	s_waitcnt lgkmcnt(1)
	v_mul_f32_e32 v3, v8, v6
	v_cndmask_b32_e64 v3, v3, -v3, s[0:1]
	s_waitcnt lgkmcnt(0)
	v_mul_f32_e32 v2, v9, v2
	v_cndmask_b32_e64 v2, v2, -v2, s[0:1]
	v_fmac_f32_e32 v3, v28, v4
	v_fmac_f32_e32 v2, v29, v5
	v_cndmask_b32_e64 v36, v28, v3, s[2:3]
	v_cndmask_b32_e64 v37, v29, v2, s[2:3]
	s_branch .LBB0_318

.LBB0_318:
	s_waitcnt vmcnt(2)
	v_add_u32_e32 v10, 0x2800, v240
	global_load_dwordx4 v[6:9], v10, s[14:15] offset:48
	global_load_dwordx4 v[14:17], v10, s[14:15] offset:32
	global_load_dwordx4 v[2:5], v10, s[14:15] offset:16
	s_nop 0
	global_load_dwordx4 v[10:13], v10, s[14:15]
	v_lshlrev_b64 v[38:39], 1, v[210:211]
	v_lshl_add_u64 v[40:41], v[20:21], 0, v[38:39]
	v_cvt_pk_bf16_f32 v22, v22, v23
	v_cvt_pk_bf16_f32 v23, v24, v25
	v_cvt_pk_bf16_f32 v24, v26, v27
	v_cvt_pk_bf16_f32 v25, v28, v29
	global_store_dwordx4 v[40:41], v[22:25], off sc1
	v_lshl_add_u64 v[26:27], v[18:19], 0, v[38:39]
	s_and_b64 vcc, exec, s[6:7]
	v_cvt_pk_bf16_f32 v22, v30, v31
	v_cvt_pk_bf16_f32 v23, v32, v33
	v_cvt_pk_bf16_f32 v24, v34, v35
	v_cvt_pk_bf16_f32 v25, v36, v37
	global_store_dwordx4 v[26:27], v[22:25], off sc1
	v_pk_mul_f32 v[26:27], v[142:143], s[26:27] op_sel_hi:[1,0]
	v_pk_mul_f32 v[28:29], v[144:145], s[26:27] op_sel_hi:[1,0]
	v_pk_mul_f32 v[22:23], v[130:131], s[26:27] op_sel_hi:[1,0]
	v_pk_mul_f32 v[24:25], v[132:133], s[26:27] op_sel_hi:[1,0]
	s_cbranch_vccnz .LBB0_320
	v_and_b32_e32 v31, 64, v239
	v_xor_b32_e32 v30, 16, v239
	v_add_u32_e32 v31, 64, v31
	v_cmp_lt_i32_e32 vcc, v30, v31
	s_nop 1
	v_cndmask_b32_e32 v30, v239, v30, vcc
	v_lshlrev_b32_e32 v36, 2, v30
	ds_bpermute_b32 v30, v36, v22
	ds_bpermute_b32 v31, v36, v23
	s_waitcnt vmcnt(4) lgkmcnt(1)
	v_mul_f32_e32 v14, v14, v30
	v_cndmask_b32_e64 v14, v14, -v14, s[0:1]
	s_waitcnt vmcnt(2)
	v_fmac_f32_e32 v14, v22, v10
	ds_bpermute_b32 v10, v36, v24
	s_waitcnt lgkmcnt(1)
	v_mul_f32_e32 v15, v15, v31
	v_cndmask_b32_e64 v30, v22, v14, s[2:3]
	v_cndmask_b32_e64 v14, v15, -v15, s[0:1]
	v_fmac_f32_e32 v14, v23, v11
	ds_bpermute_b32 v11, v36, v25
	s_waitcnt lgkmcnt(1)
	v_mul_f32_e32 v10, v16, v10
	v_cndmask_b32_e64 v10, v10, -v10, s[0:1]
	v_fmac_f32_e32 v10, v24, v12
	v_cndmask_b32_e64 v32, v24, v10, s[2:3]
	s_waitcnt lgkmcnt(0)
	v_mul_f32_e32 v10, v17, v11
	ds_bpermute_b32 v11, v36, v26
	v_cndmask_b32_e64 v10, v10, -v10, s[0:1]
	v_fmac_f32_e32 v10, v25, v13
	v_cndmask_b32_e64 v33, v25, v10, s[2:3]
	ds_bpermute_b32 v10, v36, v27
	s_waitcnt lgkmcnt(1)
	v_mul_f32_e32 v6, v6, v11
	v_cndmask_b32_e64 v6, v6, -v6, s[0:1]
	v_fmac_f32_e32 v6, v26, v2
	v_cndmask_b32_e64 v34, v26, v6, s[2:3]
	s_waitcnt lgkmcnt(0)
	v_mul_f32_e32 v2, v7, v10
	v_cndmask_b32_e64 v2, v2, -v2, s[0:1]
	v_fmac_f32_e32 v2, v27, v3
	ds_bpermute_b32 v6, v36, v28
	v_cndmask_b32_e64 v35, v27, v2, s[2:3]
	ds_bpermute_b32 v2, v36, v29
	v_cndmask_b32_e64 v31, v23, v14, s[2:3]
	s_waitcnt lgkmcnt(1)
	v_mul_f32_e32 v3, v8, v6
	v_cndmask_b32_e64 v3, v3, -v3, s[0:1]
	s_waitcnt lgkmcnt(0)
	v_mul_f32_e32 v2, v9, v2
	v_cndmask_b32_e64 v2, v2, -v2, s[0:1]
	v_fmac_f32_e32 v3, v28, v4
	v_fmac_f32_e32 v2, v29, v5
	v_cndmask_b32_e64 v36, v28, v3, s[2:3]
	v_cndmask_b32_e64 v37, v29, v2, s[2:3]
	s_branch .LBB0_321

.LBB0_321:
	s_waitcnt vmcnt(2)
	v_add_u32_e32 v10, 0x2c00, v240
	global_load_dwordx4 v[6:9], v10, s[14:15] offset:48
	global_load_dwordx4 v[14:17], v10, s[14:15] offset:32
	global_load_dwordx4 v[2:5], v10, s[14:15] offset:16
	s_nop 0
	global_load_dwordx4 v[10:13], v10, s[14:15]
	v_lshlrev_b64 v[38:39], 1, v[208:209]
	v_lshl_add_u64 v[40:41], v[20:21], 0, v[38:39]
	v_cvt_pk_bf16_f32 v22, v22, v23
	v_cvt_pk_bf16_f32 v23, v24, v25
	v_cvt_pk_bf16_f32 v24, v26, v27
	v_cvt_pk_bf16_f32 v25, v28, v29
	global_store_dwordx4 v[40:41], v[22:25], off sc1
	v_lshl_add_u64 v[26:27], v[18:19], 0, v[38:39]
	s_and_b64 vcc, exec, s[6:7]
	v_cvt_pk_bf16_f32 v22, v30, v31
	v_cvt_pk_bf16_f32 v23, v32, v33
	v_cvt_pk_bf16_f32 v24, v34, v35
	v_cvt_pk_bf16_f32 v25, v36, v37
	global_store_dwordx4 v[26:27], v[22:25], off sc1
	v_pk_mul_f32 v[26:27], v[154:155], s[26:27] op_sel_hi:[1,0]
	v_pk_mul_f32 v[28:29], v[156:157], s[26:27] op_sel_hi:[1,0]
	v_pk_mul_f32 v[22:23], v[150:151], s[26:27] op_sel_hi:[1,0]
	v_pk_mul_f32 v[24:25], v[152:153], s[26:27] op_sel_hi:[1,0]
	s_cbranch_vccnz .LBB0_323
	v_and_b32_e32 v31, 64, v239
	v_xor_b32_e32 v30, 16, v239
	v_add_u32_e32 v31, 64, v31
	v_cmp_lt_i32_e32 vcc, v30, v31
	s_nop 1
	v_cndmask_b32_e32 v30, v239, v30, vcc
	v_lshlrev_b32_e32 v30, 2, v30
	ds_bpermute_b32 v31, v30, v22
	ds_bpermute_b32 v32, v30, v23
	s_waitcnt vmcnt(4) lgkmcnt(1)
	v_mul_f32_e32 v14, v14, v31
	v_cndmask_b32_e64 v14, v14, -v14, s[0:1]
	s_waitcnt vmcnt(2)
	v_fmac_f32_e32 v14, v22, v10
	s_waitcnt lgkmcnt(0)
	v_mul_f32_e32 v15, v15, v32
	v_cndmask_b32_e64 v10, v22, v14, s[2:3]
	ds_bpermute_b32 v14, v30, v24
	v_cndmask_b32_e64 v15, v15, -v15, s[0:1]
	v_fmac_f32_e32 v15, v23, v11
	v_cndmask_b32_e64 v11, v23, v15, s[2:3]
	ds_bpermute_b32 v15, v30, v25
	s_waitcnt lgkmcnt(1)
	v_mul_f32_e32 v14, v16, v14
	v_cndmask_b32_e64 v14, v14, -v14, s[0:1]
	v_fmac_f32_e32 v14, v24, v12
	v_cndmask_b32_e64 v12, v24, v14, s[2:3]
	s_waitcnt lgkmcnt(0)
	v_mul_f32_e32 v14, v17, v15
	ds_bpermute_b32 v15, v30, v26
	v_cndmask_b32_e64 v14, v14, -v14, s[0:1]
	v_fmac_f32_e32 v14, v25, v13
	v_cndmask_b32_e64 v13, v25, v14, s[2:3]
	ds_bpermute_b32 v14, v30, v27
	s_waitcnt lgkmcnt(1)
	v_mul_f32_e32 v6, v6, v15
	v_cndmask_b32_e64 v6, v6, -v6, s[0:1]
	v_fmac_f32_e32 v6, v26, v2
	v_cndmask_b32_e64 v2, v26, v6, s[2:3]
	s_waitcnt lgkmcnt(0)
	v_mul_f32_e32 v6, v7, v14
	v_cndmask_b32_e64 v6, v6, -v6, s[0:1]
	v_fmac_f32_e32 v6, v27, v3
	ds_bpermute_b32 v7, v30, v28
	v_cndmask_b32_e64 v3, v27, v6, s[2:3]
	ds_bpermute_b32 v6, v30, v29
	s_waitcnt lgkmcnt(1)
	v_mul_f32_e32 v7, v8, v7
	v_cndmask_b32_e64 v7, v7, -v7, s[0:1]
	s_waitcnt lgkmcnt(0)
	v_mul_f32_e32 v6, v9, v6
	v_cndmask_b32_e64 v6, v6, -v6, s[0:1]
	v_fmac_f32_e32 v7, v28, v4
	v_fmac_f32_e32 v6, v29, v5
	v_cndmask_b32_e64 v4, v28, v7, s[2:3]
	v_cndmask_b32_e64 v5, v29, v6, s[2:3]
	s_branch .LBB0_324

.LBB0_324:
	v_lshlrev_b64 v[14:15], 1, v[206:207]
	v_lshl_add_u64 v[16:17], v[20:21], 0, v[14:15]
	v_cvt_pk_bf16_f32 v6, v22, v23
	v_cvt_pk_bf16_f32 v7, v24, v25
	v_cvt_pk_bf16_f32 v8, v26, v27
	v_cvt_pk_bf16_f32 v9, v28, v29
	global_store_dwordx4 v[16:17], v[6:9], off sc1
	v_lshl_add_u64 v[14:15], v[18:19], 0, v[14:15]
	s_nop 0
	v_cvt_pk_bf16_f32 v6, v10, v11
	v_cvt_pk_bf16_f32 v7, v12, v13
	v_cvt_pk_bf16_f32 v8, v2, v3
	v_cvt_pk_bf16_f32 v9, v4, v5
	global_store_dwordx4 v[14:15], v[6:9], off sc1
	s_andn2_b64 vcc, exec, s[38:39]
	s_mov_b64 s[6:7], -1
	s_cbranch_vccnz .LBB0_158
